# epilogue row-scale loads hoisted (no serialized vmcnt(0) ladder) in the three int8 row-scaled epilogues; 112 converter workgroups take all expert-weight tiles during the dense gate/up GEMM phase
# speedup vs baseline: 1.0043x; 1.0043x over previous
.LBB0_364:
	v_and_b32_e32 v2, 0xfc, v200
	v_lshrrev_b32_e32 v141, 6, v0
	s_cmpk_gt_i32 s12, 0x3f
	v_mov_b32_e32 v135, 0
	v_lshlrev_b32_e32 v136, 2, v2
	s_cbranch_scc1 .LBB0_366
	s_mul_hi_i32 s0, s12, 0x92492493
	s_add_i32 s0, s0, s12
	s_lshr_b32 s1, s0, 31
	s_ashr_i32 s0, s0, 11
	s_add_i32 s10, s0, s1
	s_mul_i32 s0, s10, 0xfffff200
	s_add_i32 s0, s0, s12
	s_mul_hi_i32 s1, s0, 0x92492493
	s_add_i32 s1, s1, s0
	s_lshr_b32 s2, s1, 31
	s_ashr_i32 s1, s1, 8
	s_add_i32 s8, s1, s2
	s_mul_i32 s1, s8, 0xfffffe40
	s_add_i32 s4, s1, s0
	s_mul_i32 s6, s8, 0x3800000
	s_mul_hi_i32 s5, s8, 0x3800000
	s_add_u32 s7, s52, s6
	s_addc_u32 s9, s53, s5
	s_lshl_b32 s0, s4, 4
	s_and_b32 s0, s0, 0xffffff80
	s_ashr_i32 s1, s0, 31
	s_lshl_b64 s[2:3], s[0:1], 13
	s_add_u32 s1, s7, s2
	s_addc_u32 s2, s9, s3
	s_lshl_b32 s3, s12, 8
	s_and_b32 s11, s3, 0x700
	s_lshl_b32 s7, s11, 2
	s_add_u32 s1, s1, s7
	s_addc_u32 s2, s2, 0
	s_mul_i32 s9, s8, 0xe00000
	s_mul_hi_i32 s7, s8, 0xe00000
	s_add_u32 s14, s88, s9
	s_addc_u32 s15, s89, s7
	s_mul_hi_i32 s7, s4, 0x92492493
	s_add_i32 s7, s7, s4
	s_lshr_b32 s9, s7, 31
	s_ashr_i32 s7, s7, 4
	s_add_i32 s7, s7, s9
	s_mul_i32 s9, s7, 0xffffffe4
	s_add_i32 s9, s9, s4
	s_add_i32 s4, s12, 0xdff
	v_readlane_b32 s16, v251, 0
	s_cmpk_lt_u32 s4, 0x1bff
	v_readlane_b32 s20, v251, 4
	v_readlane_b32 s22, v251, 6
	v_readlane_b32 s21, v251, 5
	v_readlane_b32 s23, v251, 7
	s_cselect_b32 s16, s20, s22
	s_cselect_b32 s4, s21, s23
	s_add_u32 s6, s16, s6
	v_readlane_b32 s17, v251, 1
	s_addc_u32 s4, s4, s5
	s_lshl_b32 s16, s7, 7
	s_mul_i32 s7, s7, 0x380000
	v_readlane_b32 s18, v251, 2
	s_mul_hi_i32 s5, s16, 0x7000
	s_add_u32 s17, s6, s7
	s_addc_u32 s18, s4, s5
	s_lshl_b32 s4, s9, 8
	s_ashr_i32 s5, s4, 31
	s_lshl_b64 s[6:7], s[4:5], 2
	s_add_u32 s5, s17, s6
	s_addc_u32 s6, s18, s7
	s_mul_hi_i32 s7, s8, 0x1c00000
	s_mul_i32 s8, s8, 0x1c00000
	s_add_u32 s17, s90, s8
	s_addc_u32 s7, s91, s7
	s_cmpk_lt_i32 s12, 0x1c00
	s_cselect_b32 s8, s5, s1
	s_movk_i32 s1, 0x800
	s_cselect_b32 s1, 0x1c00, s1
	v_mul_u32_u24_e32 v2, s1, v141
	s_cselect_b32 s9, s6, s2
	v_lshlrev_b32_e32 v134, 2, v2
	v_lshl_add_u64 v[2:3], s[8:9], 0, v[134:135]
	v_mov_b32_e32 v137, v135
	s_mov_b32 s3, 0
	s_cselect_b32 s10, s10, 2
	s_cselect_b32 s4, s4, s11
	s_cselect_b32 s0, s16, s0
	s_cselect_b32 s7, s7, s15
	s_cselect_b32 s6, s17, s14
	v_lshl_add_u64 v[2:3], v[2:3], 0, v[136:137]
	s_lshl_b32 s2, s1, 5
	s_waitcnt vmcnt(0)
	v_lshl_add_u64 v[10:11], v[2:3], 0, s[2:3]
	global_load_dwordx4 v[2:5], v[2:3], off nt
	s_waitcnt lgkmcnt(0)
	global_load_dwordx4 v[6:9], v[10:11], off nt
	v_lshl_add_u64 v[10:11], v[10:11], 0, s[2:3]
	v_lshl_add_u64 v[18:19], v[10:11], 0, s[2:3]
	global_load_dwordx4 v[10:13], v[10:11], off nt
	s_nop 0
	global_load_dwordx4 v[14:17], v[18:19], off nt
	v_lshl_add_u64 v[18:19], v[18:19], 0, s[2:3]
	v_lshl_add_u64 v[26:27], v[18:19], 0, s[2:3]
	global_load_dwordx4 v[18:21], v[18:19], off nt
	s_nop 0
	global_load_dwordx4 v[22:25], v[26:27], off nt
	v_lshl_add_u64 v[26:27], v[26:27], 0, s[2:3]
	v_lshl_add_u64 v[34:35], v[26:27], 0, s[2:3]
	v_lshl_add_u64 v[38:39], v[34:35], 0, s[2:3]
	v_lshl_add_u64 v[42:43], v[38:39], 0, s[2:3]
	v_lshl_add_u64 v[46:47], v[42:43], 0, s[2:3]
	v_lshl_add_u64 v[50:51], v[46:47], 0, s[2:3]
	v_lshl_add_u64 v[54:55], v[50:51], 0, s[2:3]
	v_lshl_add_u64 v[58:59], v[54:55], 0, s[2:3]
	v_lshl_add_u64 v[62:63], v[58:59], 0, s[2:3]
	global_load_dwordx4 v[26:29], v[26:27], off nt
	s_nop 0
	global_load_dwordx4 v[30:33], v[34:35], off nt
	v_readlane_b32 s19, v251, 3
	global_load_dwordx4 v[34:37], v[38:39], off nt
	s_nop 0
	global_load_dwordx4 v[38:41], v[42:43], off nt
	s_nop 0
	global_load_dwordx4 v[42:45], v[46:47], off nt
	s_nop 0
	global_load_dwordx4 v[46:49], v[50:51], off nt
	s_nop 0
	global_load_dwordx4 v[50:53], v[54:55], off nt
	s_nop 0
	global_load_dwordx4 v[54:57], v[58:59], off nt
	s_nop 0
	global_load_dwordx4 v[58:61], v[62:63], off nt
	v_lshl_add_u64 v[62:63], v[62:63], 0, s[2:3]
	global_load_dwordx4 v[62:65], v[62:63], off nt
	s_branch .LBB0_367

.LBB0_370:
	s_cmpk_gt_i32 s18, 0x3f
	s_mov_b64 s[42:43], -1
	s_cbranch_scc1 .LBB0_369
	s_add_i32 s18, s18, s13
	s_cmpk_lt_i32 s18, 0x40
	s_cselect_b64 s[44:45], -1, 0
	s_cmpk_gt_i32 s18, 0x3f
	s_cselect_b64 s[42:43], -1, 0
	s_and_b64 vcc, exec, s[42:43]
	s_cbranch_vccnz .LBB0_378
	s_mul_hi_i32 s1, s18, 0x92492493
	s_add_i32 s1, s1, s18
	s_lshr_b32 s2, s1, 31
	s_ashr_i32 s1, s1, 11
	s_add_i32 s17, s1, s2
	s_mul_i32 s1, s17, 0xfffff200
	s_add_i32 s2, s1, s18
	s_mul_hi_i32 s1, s2, 0x92492493
	s_add_i32 s1, s1, s2
	s_lshr_b32 s3, s1, 31
	s_ashr_i32 s1, s1, 8
	s_add_i32 s1, s1, s3
	s_mul_i32 s19, s1, 0xfffffe40
	s_add_i32 s19, s19, s2
	s_mov_b64 s[46:47], -1
	s_cmpk_gt_i32 s18, 0x1bff
	s_mul_hi_i32 s5, s1, 0x3800000
	s_mul_i32 s8, s1, 0x3800000
	s_cbranch_scc0 .LBB0_374
	s_add_u32 s20, s52, s8
	s_addc_u32 s21, s53, s5
	s_lshl_b32 s2, s19, 4
	s_and_b32 s14, s2, 0xffffff80
	s_ashr_i32 s15, s14, 31
	s_lshl_b64 s[2:3], s[14:15], 13
	s_add_u32 s2, s20, s2
	s_addc_u32 s3, s21, s3
	s_lshl_b32 s15, s18, 8
	s_and_b32 s36, s15, 0x700
	s_lshl_b32 s15, s36, 2
	s_add_u32 s2, s2, s15
	s_addc_u32 s3, s3, 0
	s_mul_i32 s20, s1, 0xe00000
	s_mul_hi_i32 s15, s1, 0xe00000
	s_add_u32 s40, s88, s20
	s_addc_u32 s41, s89, s15
	s_mov_b64 s[46:47], 0

.LBB0_394:
	s_andn2_b64 vcc, exec, s[44:45]
	s_waitcnt lgkmcnt(0)
	s_barrier
	s_cbranch_vccnz .LBB0_369
	s_add_i32 s18, s18, s13
	s_cmpk_gt_i32 s18, 0x3f
	s_cbranch_scc1 .LBB0_402
	s_mul_hi_i32 s0, s18, 0x92492493
	s_add_i32 s0, s0, s18
	s_lshr_b32 s1, s0, 31
	s_ashr_i32 s0, s0, 11
	s_add_i32 s10, s0, s1
	s_mul_i32 s0, s10, 0xfffff200
	s_add_i32 s0, s0, s18
	s_mul_hi_i32 s1, s0, 0x92492493
	s_add_i32 s1, s1, s0
	s_lshr_b32 s2, s1, 31
	s_ashr_i32 s8, s1, 8
	s_add_i32 s8, s8, s2
	s_mul_i32 s19, s8, 0xfffffe40
	s_add_i32 s19, s19, s0
	s_mov_b64 s[44:45], -1
	s_cmpk_gt_i32 s18, 0x1bff
	s_mul_hi_i32 s5, s8, 0x3800000
	s_mul_i32 s15, s8, 0x3800000
	s_cbranch_scc0 .LBB0_398
	s_add_u32 s4, s52, s15
	s_addc_u32 s6, s53, s5
	s_lshl_b32 s0, s19, 4
	s_and_b32 s0, s0, 0xffffff80
	s_ashr_i32 s1, s0, 31
	s_lshl_b64 s[2:3], s[0:1], 13
	s_add_u32 s1, s4, s2
	s_addc_u32 s3, s6, s3
	s_lshl_b32 s2, s18, 8
	s_and_b32 s4, s2, 0x700
	s_lshl_b32 s2, s4, 2
	s_add_u32 s2, s1, s2
	s_addc_u32 s3, s3, 0
	s_mul_i32 s6, s8, 0xe00000
	s_mul_hi_i32 s1, s8, 0xe00000
	s_add_u32 s6, s88, s6
	s_addc_u32 s7, s89, s1
	s_mov_b64 s[44:45], 0

.LBB0_543:
	v_lshl_or_b32 v152, s61, 8, v203
	v_lshl_add_u32 v146, s33, 8, v201
	v_ashrrev_i32_e32 v153, 31, v152
	v_ashrrev_i32_e32 v147, 31, v146
	s_nop 15
	s_nop 7
	v_lshl_add_u64 v[130:131], v[152:153], 2, s[6:7]
	v_lshl_add_u64 v[150:151], v[146:147], 2, s[38:39]
	global_load_dword v154, v[150:151], off
	global_load_dword v233, v[150:151], off offset:64
	global_load_dword v234, v[150:151], off offset:128
	global_load_dword v235, v[150:151], off offset:192
	global_load_dword v236, v[150:151], off offset:512
	global_load_dword v237, v[150:151], off offset:576
	global_load_dword v238, v[150:151], off offset:640
	global_load_dword v239, v[150:151], off offset:704
	global_load_dwordx4 v[142:145], v[130:131], off
	global_load_dwordx4 v[138:141], v[130:131], off offset:16
	global_load_dwordx4 v[134:137], v[130:131], off offset:512
	s_nop 0
	global_load_dwordx4 v[130:133], v[130:131], off offset:528
	v_cvt_f32_i32_e32 v157, v19
	v_cvt_f32_i32_e32 v156, v18
	v_cvt_f32_i32_e32 v159, v21
	v_cvt_f32_i32_e32 v158, v20
	v_cvt_f32_i32_e32 v161, v23
	v_cvt_f32_i32_e32 v160, v22
	v_cvt_f32_i32_e32 v163, v25
	v_cvt_f32_i32_e32 v162, v24
	v_cvt_f32_i32_e32 v165, v27
	v_cvt_f32_i32_e32 v164, v26
	v_cvt_f32_i32_e32 v167, v29
	v_cvt_f32_i32_e32 v166, v28
	v_cvt_f32_i32_e32 v169, v35
	v_cvt_f32_i32_e32 v168, v34
	v_cvt_f32_i32_e32 v171, v37
	v_cvt_f32_i32_e32 v170, v36
	v_mov_b64_e32 v[148:149], s[36:37]
	v_mad_i64_i32 v[172:173], s[2:3], v146, s31, v[148:149]
	v_or_b32_e32 v174, 16, v146
	v_lshlrev_b64 v[152:153], 1, v[152:153]
	v_ashrrev_i32_e32 v175, 31, v174
	v_lshl_add_u64 v[172:173], v[172:173], 0, v[152:153]
	v_lshl_add_u64 v[176:177], v[174:175], 2, s[38:39]
	v_mad_i64_i32 v[174:175], s[2:3], v174, s31, v[148:149]
	v_lshl_add_u64 v[174:175], v[174:175], 0, v[152:153]
	v_add_u32_e32 v147, 0x80, v146
	s_andn2_b64 vcc, exec, s[42:43]
	s_waitcnt vmcnt(0)
	v_pk_mul_f32 v[178:179], v[142:143], v[154:155] op_sel_hi:[1,0]
	v_pk_mul_f32 v[180:181], v[144:145], v[154:155] op_sel_hi:[1,0]
	v_pk_mul_f32 v[182:183], v[138:139], v[154:155] op_sel_hi:[1,0]
	v_pk_mul_f32 v[184:185], v[140:141], v[154:155] op_sel_hi:[1,0]
	v_pk_mul_f32 v[186:187], v[134:135], v[154:155] op_sel_hi:[1,0]
	v_pk_mul_f32 v[188:189], v[136:137], v[154:155] op_sel_hi:[1,0]
	v_pk_mul_f32 v[190:191], v[130:131], v[154:155] op_sel_hi:[1,0]
	v_pk_mul_f32 v[154:155], v[132:133], v[154:155] op_sel_hi:[1,0]
	v_pk_mul_f32 v[158:159], v[180:181], v[158:159]
	v_pk_mul_f32 v[156:157], v[178:179], v[156:157]
	v_pk_mul_f32 v[162:163], v[184:185], v[162:163]
	v_pk_mul_f32 v[160:161], v[182:183], v[160:161]
	v_pk_mul_f32 v[166:167], v[188:189], v[166:167]
	v_pk_mul_f32 v[164:165], v[186:187], v[164:165]
	v_pk_mul_f32 v[170:171], v[154:155], v[170:171]
	v_pk_mul_f32 v[168:169], v[190:191], v[168:169]
	v_cvt_pk_bf16_f32 v154, v156, v157
	v_cvt_pk_bf16_f32 v155, v158, v159
	v_cvt_pk_bf16_f32 v156, v160, v161
	v_cvt_pk_bf16_f32 v157, v162, v163
	v_cvt_pk_bf16_f32 v158, v164, v165
	v_cvt_pk_bf16_f32 v159, v166, v167
	v_cvt_pk_bf16_f32 v160, v168, v169
	v_cvt_pk_bf16_f32 v161, v170, v171
	global_store_dwordx4 v[172:173], v[154:157], off
	global_store_dwordx4 v[172:173], v[158:161], off offset:256
	v_cvt_f32_i32_e32 v157, v51
	v_cvt_f32_i32_e32 v156, v50
	v_cvt_f32_i32_e32 v159, v53
	v_cvt_f32_i32_e32 v158, v52
	v_cvt_f32_i32_e32 v161, v63
	v_cvt_f32_i32_e32 v160, v62
	v_cvt_f32_i32_e32 v163, v65
	v_cvt_f32_i32_e32 v162, v64
	v_cvt_f32_i32_e32 v165, v55
	v_cvt_f32_i32_e32 v164, v54
	v_cvt_f32_i32_e32 v167, v57
	v_cvt_f32_i32_e32 v166, v56
	v_cvt_f32_i32_e32 v169, v67
	v_cvt_f32_i32_e32 v168, v66
	v_cvt_f32_i32_e32 v171, v69
	v_cvt_f32_i32_e32 v170, v68
	v_or_b32_e32 v172, 32, v146
	v_ashrrev_i32_e32 v173, 31, v172
	v_lshl_add_u64 v[176:177], v[172:173], 2, s[38:39]
	v_mad_i64_i32 v[172:173], s[2:3], v172, s31, v[148:149]
	v_lshl_add_u64 v[172:173], v[172:173], 0, v[152:153]
	v_mov_b32_e32 v154, v233
	v_pk_mul_f32 v[178:179], v[142:143], v[154:155] op_sel_hi:[1,0]
	v_pk_mul_f32 v[180:181], v[144:145], v[154:155] op_sel_hi:[1,0]
	v_pk_mul_f32 v[182:183], v[138:139], v[154:155] op_sel_hi:[1,0]
	v_pk_mul_f32 v[184:185], v[140:141], v[154:155] op_sel_hi:[1,0]
	v_pk_mul_f32 v[186:187], v[134:135], v[154:155] op_sel_hi:[1,0]
	v_pk_mul_f32 v[188:189], v[136:137], v[154:155] op_sel_hi:[1,0]
	v_pk_mul_f32 v[190:191], v[130:131], v[154:155] op_sel_hi:[1,0]
	v_pk_mul_f32 v[154:155], v[132:133], v[154:155] op_sel_hi:[1,0]
	v_pk_mul_f32 v[158:159], v[180:181], v[158:159]
	v_pk_mul_f32 v[156:157], v[178:179], v[156:157]
	v_pk_mul_f32 v[162:163], v[184:185], v[162:163]
	v_pk_mul_f32 v[160:161], v[182:183], v[160:161]
	v_pk_mul_f32 v[166:167], v[188:189], v[166:167]
	v_pk_mul_f32 v[164:165], v[186:187], v[164:165]
	v_pk_mul_f32 v[170:171], v[154:155], v[170:171]
	v_pk_mul_f32 v[168:169], v[190:191], v[168:169]
	v_cvt_pk_bf16_f32 v154, v156, v157
	v_cvt_pk_bf16_f32 v155, v158, v159
	v_cvt_pk_bf16_f32 v156, v160, v161
	v_cvt_pk_bf16_f32 v157, v162, v163
	v_cvt_pk_bf16_f32 v158, v164, v165
	v_cvt_pk_bf16_f32 v159, v166, v167
	v_cvt_pk_bf16_f32 v160, v168, v169
	v_cvt_pk_bf16_f32 v161, v170, v171
	global_store_dwordx4 v[174:175], v[154:157], off
	global_store_dwordx4 v[174:175], v[158:161], off offset:256
	v_cvt_f32_i32_e32 v157, v83
	v_cvt_f32_i32_e32 v156, v82
	v_cvt_f32_i32_e32 v159, v85
	v_cvt_f32_i32_e32 v158, v84
	v_cvt_f32_i32_e32 v161, v95
	v_cvt_f32_i32_e32 v160, v94
	v_cvt_f32_i32_e32 v163, v97
	v_cvt_f32_i32_e32 v162, v96
	v_cvt_f32_i32_e32 v165, v87
	v_cvt_f32_i32_e32 v164, v86
	v_cvt_f32_i32_e32 v167, v89
	v_cvt_f32_i32_e32 v166, v88
	v_cvt_f32_i32_e32 v169, v99
	v_cvt_f32_i32_e32 v168, v98
	v_cvt_f32_i32_e32 v171, v101
	v_cvt_f32_i32_e32 v170, v100
	v_or_b32_e32 v174, 48, v146
	v_ashrrev_i32_e32 v175, 31, v174
	v_lshl_add_u64 v[176:177], v[174:175], 2, s[38:39]
	v_mov_b32_e32 v154, v234
	v_pk_mul_f32 v[178:179], v[142:143], v[154:155] op_sel_hi:[1,0]
	v_pk_mul_f32 v[180:181], v[144:145], v[154:155] op_sel_hi:[1,0]
	v_pk_mul_f32 v[182:183], v[138:139], v[154:155] op_sel_hi:[1,0]
	v_pk_mul_f32 v[184:185], v[140:141], v[154:155] op_sel_hi:[1,0]
	v_pk_mul_f32 v[186:187], v[134:135], v[154:155] op_sel_hi:[1,0]
	v_pk_mul_f32 v[188:189], v[136:137], v[154:155] op_sel_hi:[1,0]
	v_pk_mul_f32 v[190:191], v[130:131], v[154:155] op_sel_hi:[1,0]
	v_pk_mul_f32 v[154:155], v[132:133], v[154:155] op_sel_hi:[1,0]
	v_pk_mul_f32 v[158:159], v[180:181], v[158:159]
	v_pk_mul_f32 v[156:157], v[178:179], v[156:157]
	v_pk_mul_f32 v[162:163], v[184:185], v[162:163]
	v_pk_mul_f32 v[160:161], v[182:183], v[160:161]
	v_pk_mul_f32 v[166:167], v[188:189], v[166:167]
	v_pk_mul_f32 v[164:165], v[186:187], v[164:165]
	v_pk_mul_f32 v[170:171], v[154:155], v[170:171]
	v_pk_mul_f32 v[168:169], v[190:191], v[168:169]
	v_cvt_pk_bf16_f32 v154, v156, v157
	v_cvt_pk_bf16_f32 v155, v158, v159
	v_cvt_pk_bf16_f32 v156, v160, v161
	v_cvt_pk_bf16_f32 v157, v162, v163
	v_cvt_pk_bf16_f32 v158, v164, v165
	v_cvt_pk_bf16_f32 v159, v166, v167
	v_cvt_pk_bf16_f32 v160, v168, v169
	v_cvt_pk_bf16_f32 v161, v170, v171
	global_store_dwordx4 v[172:173], v[154:157], off
	global_store_dwordx4 v[172:173], v[158:161], off offset:256
	v_cvt_f32_i32_e32 v157, v115
	v_cvt_f32_i32_e32 v156, v114
	v_cvt_f32_i32_e32 v159, v117
	v_cvt_f32_i32_e32 v158, v116
	v_cvt_f32_i32_e32 v161, v123
	v_cvt_f32_i32_e32 v160, v122
	v_cvt_f32_i32_e32 v163, v125
	v_cvt_f32_i32_e32 v162, v124
	v_cvt_f32_i32_e32 v165, v119
	v_cvt_f32_i32_e32 v164, v118
	v_cvt_f32_i32_e32 v167, v121
	v_cvt_f32_i32_e32 v166, v120
	v_cvt_f32_i32_e32 v169, v127
	v_cvt_f32_i32_e32 v168, v126
	v_cvt_f32_i32_e32 v171, v129
	v_cvt_f32_i32_e32 v170, v128
	v_mad_i64_i32 v[172:173], s[2:3], v174, s31, v[148:149]
	v_lshl_add_u64 v[172:173], v[172:173], 0, v[152:153]
	v_mov_b32_e32 v154, v235
	v_pk_mul_f32 v[174:175], v[142:143], v[154:155] op_sel_hi:[1,0]
	v_pk_mul_f32 v[176:177], v[144:145], v[154:155] op_sel_hi:[1,0]
	v_pk_mul_f32 v[178:179], v[138:139], v[154:155] op_sel_hi:[1,0]
	v_pk_mul_f32 v[180:181], v[140:141], v[154:155] op_sel_hi:[1,0]
	v_pk_mul_f32 v[182:183], v[134:135], v[154:155] op_sel_hi:[1,0]
	v_pk_mul_f32 v[184:185], v[136:137], v[154:155] op_sel_hi:[1,0]
	v_pk_mul_f32 v[186:187], v[130:131], v[154:155] op_sel_hi:[1,0]
	v_pk_mul_f32 v[154:155], v[132:133], v[154:155] op_sel_hi:[1,0]
	v_pk_mul_f32 v[158:159], v[176:177], v[158:159]
	v_pk_mul_f32 v[156:157], v[174:175], v[156:157]
	v_pk_mul_f32 v[162:163], v[180:181], v[162:163]
	v_pk_mul_f32 v[160:161], v[178:179], v[160:161]
	v_pk_mul_f32 v[166:167], v[184:185], v[166:167]
	v_pk_mul_f32 v[164:165], v[182:183], v[164:165]
	v_pk_mul_f32 v[170:171], v[154:155], v[170:171]
	v_pk_mul_f32 v[168:169], v[186:187], v[168:169]
	v_cvt_pk_bf16_f32 v154, v156, v157
	v_cvt_pk_bf16_f32 v155, v158, v159
	v_cvt_pk_bf16_f32 v156, v160, v161
	v_cvt_pk_bf16_f32 v157, v162, v163
	v_cvt_pk_bf16_f32 v158, v164, v165
	v_cvt_pk_bf16_f32 v159, v166, v167
	v_cvt_pk_bf16_f32 v160, v168, v169
	v_cvt_pk_bf16_f32 v161, v170, v171
	global_store_dwordx4 v[172:173], v[154:157], off
	global_store_dwordx4 v[172:173], v[158:161], off offset:256
	v_cvt_f32_i32_e32 v157, v3
	v_cvt_f32_i32_e32 v156, v2
	v_cvt_f32_i32_e32 v159, v5
	v_cvt_f32_i32_e32 v158, v4
	v_cvt_f32_i32_e32 v161, v7
	v_cvt_f32_i32_e32 v160, v6
	v_cvt_f32_i32_e32 v163, v9
	v_cvt_f32_i32_e32 v162, v8
	v_cvt_f32_i32_e32 v165, v11
	v_cvt_f32_i32_e32 v164, v10
	v_cvt_f32_i32_e32 v167, v13
	v_cvt_f32_i32_e32 v166, v12
	v_cvt_f32_i32_e32 v169, v15
	v_cvt_f32_i32_e32 v168, v14
	v_cvt_f32_i32_e32 v171, v17
	v_cvt_f32_i32_e32 v170, v16
	v_mad_i64_i32 v[172:173], s[2:3], v147, s31, v[148:149]
	v_lshl_add_u64 v[172:173], v[172:173], 0, v[152:153]
	v_add_u32_e32 v147, 0x90, v146
	v_mov_b32_e32 v154, v236
	v_pk_mul_f32 v[174:175], v[142:143], v[154:155] op_sel_hi:[1,0]
	v_pk_mul_f32 v[176:177], v[144:145], v[154:155] op_sel_hi:[1,0]
	v_pk_mul_f32 v[178:179], v[138:139], v[154:155] op_sel_hi:[1,0]
	v_pk_mul_f32 v[180:181], v[140:141], v[154:155] op_sel_hi:[1,0]
	v_pk_mul_f32 v[182:183], v[134:135], v[154:155] op_sel_hi:[1,0]
	v_pk_mul_f32 v[184:185], v[136:137], v[154:155] op_sel_hi:[1,0]
	v_pk_mul_f32 v[186:187], v[130:131], v[154:155] op_sel_hi:[1,0]
	v_pk_mul_f32 v[154:155], v[132:133], v[154:155] op_sel_hi:[1,0]
	v_pk_mul_f32 v[158:159], v[176:177], v[158:159]
	v_pk_mul_f32 v[156:157], v[174:175], v[156:157]
	v_pk_mul_f32 v[162:163], v[180:181], v[162:163]
	v_pk_mul_f32 v[160:161], v[178:179], v[160:161]
	v_pk_mul_f32 v[166:167], v[184:185], v[166:167]
	v_pk_mul_f32 v[164:165], v[182:183], v[164:165]
	v_pk_mul_f32 v[170:171], v[154:155], v[170:171]
	v_pk_mul_f32 v[168:169], v[186:187], v[168:169]
	v_cvt_pk_bf16_f32 v154, v156, v157
	v_cvt_pk_bf16_f32 v155, v158, v159
	v_cvt_pk_bf16_f32 v156, v160, v161
	v_cvt_pk_bf16_f32 v157, v162, v163
	v_cvt_pk_bf16_f32 v158, v164, v165
	v_cvt_pk_bf16_f32 v159, v166, v167
	v_cvt_pk_bf16_f32 v160, v168, v169
	v_cvt_pk_bf16_f32 v161, v170, v171
	global_store_dwordx4 v[172:173], v[154:157], off
	global_store_dwordx4 v[172:173], v[158:161], off offset:256
	v_cvt_f32_i32_e32 v157, v31
	v_cvt_f32_i32_e32 v156, v30
	v_cvt_f32_i32_e32 v159, v33
	v_cvt_f32_i32_e32 v158, v32
	v_cvt_f32_i32_e32 v161, v43
	v_cvt_f32_i32_e32 v160, v42
	v_cvt_f32_i32_e32 v163, v45
	v_cvt_f32_i32_e32 v162, v44
	v_cvt_f32_i32_e32 v165, v39
	v_cvt_f32_i32_e32 v164, v38
	v_cvt_f32_i32_e32 v167, v41
	v_cvt_f32_i32_e32 v166, v40
	v_cvt_f32_i32_e32 v169, v47
	v_cvt_f32_i32_e32 v168, v46
	v_cvt_f32_i32_e32 v171, v49
	v_cvt_f32_i32_e32 v170, v48
	v_mad_i64_i32 v[172:173], s[2:3], v147, s31, v[148:149]
	v_lshl_add_u64 v[172:173], v[172:173], 0, v[152:153]
	v_add_u32_e32 v147, 0xa0, v146
	v_add_u32_e32 v146, 0xb0, v146
	v_mov_b32_e32 v154, v237
	v_pk_mul_f32 v[174:175], v[142:143], v[154:155] op_sel_hi:[1,0]
	v_pk_mul_f32 v[176:177], v[144:145], v[154:155] op_sel_hi:[1,0]
	v_pk_mul_f32 v[178:179], v[138:139], v[154:155] op_sel_hi:[1,0]
	v_pk_mul_f32 v[180:181], v[140:141], v[154:155] op_sel_hi:[1,0]
	v_pk_mul_f32 v[182:183], v[134:135], v[154:155] op_sel_hi:[1,0]
	v_pk_mul_f32 v[184:185], v[136:137], v[154:155] op_sel_hi:[1,0]
	v_pk_mul_f32 v[186:187], v[130:131], v[154:155] op_sel_hi:[1,0]
	v_pk_mul_f32 v[154:155], v[132:133], v[154:155] op_sel_hi:[1,0]
	v_pk_mul_f32 v[158:159], v[176:177], v[158:159]
	v_pk_mul_f32 v[156:157], v[174:175], v[156:157]
	v_pk_mul_f32 v[162:163], v[180:181], v[162:163]
	v_pk_mul_f32 v[160:161], v[178:179], v[160:161]
	v_pk_mul_f32 v[166:167], v[184:185], v[166:167]
	v_pk_mul_f32 v[164:165], v[182:183], v[164:165]
	v_pk_mul_f32 v[170:171], v[154:155], v[170:171]
	v_pk_mul_f32 v[168:169], v[186:187], v[168:169]
	v_cvt_pk_bf16_f32 v154, v156, v157
	v_cvt_pk_bf16_f32 v155, v158, v159
	v_cvt_pk_bf16_f32 v156, v160, v161
	v_cvt_pk_bf16_f32 v157, v162, v163
	v_cvt_pk_bf16_f32 v158, v164, v165
	v_cvt_pk_bf16_f32 v159, v166, v167
	v_cvt_pk_bf16_f32 v160, v168, v169
	v_cvt_pk_bf16_f32 v161, v170, v171
	global_store_dwordx4 v[172:173], v[154:157], off
	global_store_dwordx4 v[172:173], v[158:161], off offset:256
	v_cvt_f32_i32_e32 v157, v59
	v_cvt_f32_i32_e32 v156, v58
	v_cvt_f32_i32_e32 v159, v61
	v_cvt_f32_i32_e32 v158, v60
	v_cvt_f32_i32_e32 v161, v75
	v_cvt_f32_i32_e32 v160, v74
	v_cvt_f32_i32_e32 v163, v77
	v_cvt_f32_i32_e32 v162, v76
	v_cvt_f32_i32_e32 v165, v71
	v_cvt_f32_i32_e32 v164, v70
	v_cvt_f32_i32_e32 v167, v73
	v_cvt_f32_i32_e32 v166, v72
	v_cvt_f32_i32_e32 v169, v79
	v_cvt_f32_i32_e32 v168, v78
	v_cvt_f32_i32_e32 v171, v81
	v_cvt_f32_i32_e32 v170, v80
	v_mad_i64_i32 v[172:173], s[2:3], v147, s31, v[148:149]
	v_lshl_add_u64 v[172:173], v[172:173], 0, v[152:153]
	v_mad_i64_i32 v[146:147], s[2:3], v146, s31, v[148:149]
	v_lshl_add_u64 v[146:147], v[146:147], 0, v[152:153]
	s_mov_b64 s[2:3], -1
	v_mov_b32_e32 v154, v238
	v_pk_mul_f32 v[174:175], v[142:143], v[154:155] op_sel_hi:[1,0]
	v_pk_mul_f32 v[176:177], v[144:145], v[154:155] op_sel_hi:[1,0]
	v_pk_mul_f32 v[178:179], v[138:139], v[154:155] op_sel_hi:[1,0]
	v_pk_mul_f32 v[180:181], v[140:141], v[154:155] op_sel_hi:[1,0]
	v_pk_mul_f32 v[182:183], v[134:135], v[154:155] op_sel_hi:[1,0]
	v_pk_mul_f32 v[184:185], v[136:137], v[154:155] op_sel_hi:[1,0]
	v_pk_mul_f32 v[186:187], v[130:131], v[154:155] op_sel_hi:[1,0]
	v_pk_mul_f32 v[154:155], v[132:133], v[154:155] op_sel_hi:[1,0]
	v_pk_mul_f32 v[158:159], v[176:177], v[158:159]
	v_pk_mul_f32 v[156:157], v[174:175], v[156:157]
	v_pk_mul_f32 v[162:163], v[180:181], v[162:163]
	v_pk_mul_f32 v[160:161], v[178:179], v[160:161]
	v_pk_mul_f32 v[166:167], v[184:185], v[166:167]
	v_pk_mul_f32 v[164:165], v[182:183], v[164:165]
	v_pk_mul_f32 v[170:171], v[154:155], v[170:171]
	v_pk_mul_f32 v[168:169], v[186:187], v[168:169]
	v_cvt_pk_bf16_f32 v154, v156, v157
	v_cvt_pk_bf16_f32 v155, v158, v159
	v_cvt_pk_bf16_f32 v156, v160, v161
	v_cvt_pk_bf16_f32 v157, v162, v163
	v_cvt_pk_bf16_f32 v158, v164, v165
	v_cvt_pk_bf16_f32 v159, v166, v167
	v_cvt_pk_bf16_f32 v160, v168, v169
	v_cvt_pk_bf16_f32 v161, v170, v171
	global_store_dwordx4 v[172:173], v[154:157], off
	global_store_dwordx4 v[172:173], v[158:161], off offset:256
	v_cvt_f32_i32_e32 v155, v91
	v_cvt_f32_i32_e32 v154, v90
	v_cvt_f32_i32_e32 v157, v93
	v_cvt_f32_i32_e32 v156, v92
	v_cvt_f32_i32_e32 v159, v107
	v_cvt_f32_i32_e32 v158, v106
	v_cvt_f32_i32_e32 v161, v109
	v_cvt_f32_i32_e32 v160, v108
	v_cvt_f32_i32_e32 v163, v103
	v_cvt_f32_i32_e32 v162, v102
	v_cvt_f32_i32_e32 v165, v105
	v_cvt_f32_i32_e32 v164, v104
	v_cvt_f32_i32_e32 v167, v111
	v_cvt_f32_i32_e32 v166, v110
	v_cvt_f32_i32_e32 v169, v113
	v_cvt_f32_i32_e32 v168, v112
	v_mov_b32_e32 v150, v239
	v_pk_mul_f32 v[142:143], v[142:143], v[150:151] op_sel_hi:[1,0]
	v_pk_mul_f32 v[144:145], v[144:145], v[150:151] op_sel_hi:[1,0]
	v_pk_mul_f32 v[138:139], v[138:139], v[150:151] op_sel_hi:[1,0]
	v_pk_mul_f32 v[140:141], v[140:141], v[150:151] op_sel_hi:[1,0]
	v_pk_mul_f32 v[134:135], v[134:135], v[150:151] op_sel_hi:[1,0]
	v_pk_mul_f32 v[136:137], v[136:137], v[150:151] op_sel_hi:[1,0]
	v_pk_mul_f32 v[130:131], v[130:131], v[150:151] op_sel_hi:[1,0]
	v_pk_mul_f32 v[132:133], v[132:133], v[150:151] op_sel_hi:[1,0]
	v_pk_mul_f32 v[144:145], v[144:145], v[156:157]
	v_pk_mul_f32 v[142:143], v[142:143], v[154:155]
	v_pk_mul_f32 v[140:141], v[140:141], v[160:161]
	v_pk_mul_f32 v[138:139], v[138:139], v[158:159]
	v_pk_mul_f32 v[136:137], v[136:137], v[164:165]
	v_pk_mul_f32 v[134:135], v[134:135], v[162:163]
	v_pk_mul_f32 v[148:149], v[132:133], v[168:169]
	v_pk_mul_f32 v[150:151], v[130:131], v[166:167]
	v_cvt_pk_bf16_f32 v130, v142, v143
	v_cvt_pk_bf16_f32 v131, v144, v145
	v_cvt_pk_bf16_f32 v132, v138, v139
	v_cvt_pk_bf16_f32 v133, v140, v141
	v_cvt_pk_bf16_f32 v134, v134, v135
	v_cvt_pk_bf16_f32 v135, v136, v137
	v_cvt_pk_bf16_f32 v136, v150, v151
	v_cvt_pk_bf16_f32 v137, v148, v149
	global_store_dwordx4 v[146:147], v[130:133], off
	global_store_dwordx4 v[146:147], v[134:137], off offset:256
	s_cbranch_vccnz .LBB0_525
	s_andn2_b64 vcc, exec, s[4:5]
	s_cbranch_vccnz .LBB0_524
	s_barrier
	s_branch .LBB0_524

.LBB0_839:
	s_add_u32 s16, s56, 0x3eb00000
	s_addc_u32 s17, s57, 0
	s_cmp_lt_i32 s58, 8
	s_cselect_b64 s[0:1], -1, 0
	s_cmp_gt_i32 s59, 7
	s_cselect_b64 s[2:3], -1, 0
	s_and_b64 s[0:1], s[0:1], s[2:3]
	s_andn2_b64 vcc, exec, s[0:1]
	s_cbranch_vccnz .LBB0_921
	s_mov_b32 s99, s13
	s_cmp_lt_u32 s12, 144
	s_cbranch_scc1 .Lsp7_gemm
	s_mov_b32 s98, s12
	s_add_i32 s12, s12, -80
	s_mov_b32 s13, 112
	v_lshrrev_b32_e32 v140, 3, v0
	s_add_u32 s0, s94, 0xffffffe0
	s_addc_u32 s1, s95, -1
	s_load_dwordx2 s[52:53], s[0:1], 0x0
	s_waitcnt lgkmcnt(0)
	s_branch .Lcv_364
.Lsp7_gemm:
	s_mov_b32 s13, 144
	s_cmpk_gt_i32 s12, 0xaff
	v_readfirstlane_b32 s3, v0
	s_cbranch_scc1 .LBB0_867
	v_lshlrev_b32_e32 v2, 4, v0
	v_and_b32_e32 v3, 32, v0
	v_bitop3_b32 v2, v2, v3, 48 bitop3:0x6c
	v_lshrrev_b32_e32 v3, 1, v0
	v_lshrrev_b32_e32 v5, 5, v0
	v_and_b32_e32 v3, 24, v3
	v_and_b32_e32 v5, 4, v5
	s_waitcnt vmcnt(14)
	v_bfe_u32 v6, v0, 2, 2
	v_bfe_u32 v4, v0, 2, 4
	v_or3_b32 v3, v5, v6, v3
	v_lshrrev_b32_e32 v5, 3, v0
	v_and_or_b32 v2, v0, 64, v2
	v_and_or_b32 v6, v5, 48, v4
	v_and_or_b32 v5, v5, 32, v3
	s_lshr_b32 s6, s3, 6
	v_lshl_or_b32 v202, v5, 11, v2
	v_bfe_u32 v5, v0, 3, 25
	s_lshr_b32 s14, s3, 8
	s_lshl_b32 s10, s6, 10
	v_or_b32_e32 v5, 64, v5
	s_movk_i32 s0, 0x70
	s_add_u32 s11, s56, 0x4db00000
	v_and_or_b32 v4, v5, s0, v4
	s_movk_i32 s0, 0x60
	s_addc_u32 s18, s57, 0
	s_ashr_i32 s19, s12, 31
	v_and_or_b32 v3, v5, s0, v3
	s_lshr_b32 s0, s19, 29
	s_add_i32 s0, s12, s0
	s_ashr_i32 s1, s0, 3
	s_and_b32 s0, s0, -8
	s_sub_i32 s0, s12, s0
	s_cmp_lt_i32 s0, 0
	s_movk_i32 s20, 0x161
	s_cselect_b32 s2, s20, 0x160
	s_mul_i32 s0, s0, s2
	s_add_i32 s0, s0, s1
	s_mul_hi_i32 s1, s0, 0x2e8ba2e9
	s_lshr_b32 s2, s1, 31
	s_ashr_i32 s1, s1, 6
	s_add_i32 s1, s1, s2
	s_lshl_b32 s4, s1, 3
	s_mulk_i32 s1, 0x160
	s_sub_i32 s0, s0, s1
	s_sext_i32_i16 s1, s0
	s_bfe_u32 s1, s1, 0x3001c
	s_add_i32 s1, s0, s1
	s_sext_i32_i16 s2, s1
	s_and_b32 s1, s1, 0xfff8
	s_sub_i32 s0, s0, s1
	s_sext_i32_i16 s0, s0
	s_add_i32 s0, s4, s0
	s_ashr_i32 s1, s0, 31
	s_lshr_b32 s2, s2, 3
	s_lshl_b64 s[4:5], s[0:1], 19
	s_add_u32 s26, s24, s4
	s_addc_u32 s27, s25, s5
	s_bfe_i64 s[4:5], s[2:3], 0x100000
	s_lshl_b64 s[4:5], s[4:5], 19
	s_add_u32 s8, s11, s4
	s_addc_u32 s9, s18, s5
	s_add_i32 s1, s10, 0
	v_lshl_or_b32 v201, v6, 11, v2
	v_lshl_or_b32 v203, v4, 11, v2
	v_lshl_or_b32 v204, v3, 11, v2
	s_mov_b64 s[4:5], s[8:9]
	s_add_i32 s21, s1, 0x10000
	v_mov_b32_e32 v2, v202
	s_mov_b32 m0, s21
	s_add_i32 s33, s1, 0x12000
	global_load_lds_dwordx4 v2, s[4:5]
	v_mov_b32_e32 v2, v204
	s_mov_b32 m0, s33
	s_mov_b32 s7, 0
	global_load_lds_dwordx4 v2, s[4:5]
	s_add_u32 s4, s8, 0x40000
	s_addc_u32 s5, s9, 0
	s_add_i32 s35, s1, 0x14000
	v_mov_b32_e32 v2, v202
	s_mov_b32 m0, s35
	s_add_i32 s60, s1, 0x16000
	global_load_lds_dwordx4 v2, s[4:5]
	v_mov_b32_e32 v2, v204
	s_mov_b32 m0, s60
	s_add_i32 s61, s1, 0x2000
	global_load_lds_dwordx4 v2, s[4:5]
	s_mov_b64 s[4:5], s[26:27]
	v_mov_b32_e32 v2, v201
	s_mov_b32 m0, s1
	s_nop 0
	global_load_lds_dwordx4 v2, s[4:5]
	v_mov_b32_e32 v2, v203
	s_mov_b32 m0, s61
	s_nop 0
	global_load_lds_dwordx4 v2, s[4:5]
	s_add_u32 s4, s26, 0x40000
	s_addc_u32 s5, s27, 0
	s_add_i32 s62, s1, 0x4000
	v_mov_b32_e32 v2, v201
	s_mov_b32 m0, s62
	s_add_i32 s63, s1, 0x6000
	global_load_lds_dwordx4 v2, s[4:5]
	v_mov_b32_e32 v2, v203
	s_mov_b32 m0, s63
	s_cmp_eq_u32 s14, 1
	global_load_lds_dwordx4 v2, s[4:5]
	s_cselect_b64 s[4:5], -1, 0
	s_cmp_lg_u32 s14, 1
	s_cbranch_scc1 .LBB0_843
	s_barrier

.LBB0_863:
	s_lshl_b32 s2, s73, 8
	v_lshl_add_u32 v146, s72, 8, v205
	s_ashr_i32 s3, s2, 31
	v_ashrrev_i32_e32 v147, 31, v146
	s_nop 15
	s_nop 7
	v_lshl_add_u64 v[138:139], s[2:3], 2, v[194:195]
	v_lshl_add_u64 v[146:147], v[146:147], 2, s[38:39]
	global_load_dwordx4 v[142:145], v[138:139], off
	global_load_dwordx4 v[134:137], v[138:139], off offset:16
	global_load_dwordx4 v[130:133], v[138:139], off offset:528
	s_nop 0
	global_load_dwordx4 v[138:141], v[138:139], off offset:512
	v_cvt_f32_i32_e32 v149, v19
	global_load_dword v167, v[146:147], off
	global_load_dword v233, v[146:147], off offset:64
	global_load_dword v234, v[146:147], off offset:128
	global_load_dword v235, v[146:147], off offset:192
	global_load_dword v236, v[146:147], off offset:512
	global_load_dword v237, v[146:147], off offset:576
	global_load_dword v238, v[146:147], off offset:640
	global_load_dword v239, v[146:147], off offset:704
	v_cvt_f32_i32_e32 v148, v18
	v_cvt_f32_i32_e32 v151, v21
	v_cvt_f32_i32_e32 v150, v20
	v_cvt_f32_i32_e32 v153, v23
	v_cvt_f32_i32_e32 v152, v22
	v_cvt_f32_i32_e32 v155, v25
	v_cvt_f32_i32_e32 v154, v24
	v_cvt_f32_i32_e32 v157, v27
	v_cvt_f32_i32_e32 v156, v26
	v_cvt_f32_i32_e32 v159, v29
	v_cvt_f32_i32_e32 v158, v28
	v_cvt_f32_i32_e32 v163, v37
	v_cvt_f32_i32_e32 v162, v36
	v_cvt_f32_i32_e32 v161, v35
	v_cvt_f32_i32_e32 v160, v34
	v_mov_b32_e32 v164, 0
	v_mov_b32_e32 v165, 0
	s_mul_i32 s2, s72, 0x58
	s_add_i32 s2, s2, s73
	s_ashr_i32 s3, s2, 31
	s_waitcnt vmcnt(0)
	v_pk_mul_f32 v[150:151], v[144:145], v[150:151]
	v_pk_mul_f32 v[148:149], v[142:143], v[148:149]
	v_pk_mul_f32 v[154:155], v[136:137], v[154:155]
	v_pk_mul_f32 v[152:153], v[134:135], v[152:153]
	v_pk_mul_f32 v[158:159], v[140:141], v[158:159]
	v_mul_f32_e32 v166, 0xbfb8aa3b, v167
	v_mul_f32_e32 v167, v167, v167
	v_pk_mul_f32 v[156:157], v[138:139], v[156:157]
	v_pk_mul_f32 v[162:163], v[132:133], v[162:163]
	v_div_scale_f32 v170, s[30:31], v167, v167, 1.0
	v_pk_mul_f32 v[168:169], v[148:149], v[166:167] op_sel_hi:[1,0]
	v_pk_mul_f32 v[158:159], v[150:151], v[158:159]
	v_pk_mul_f32 v[148:149], v[148:149], v[156:157]
	v_pk_mul_f32 v[150:151], v[150:151], v[166:167] op_sel_hi:[1,0]
	v_pk_mul_f32 v[156:157], v[152:153], v[166:167] op_sel_hi:[1,0]
	v_pk_mul_f32 v[162:163], v[154:155], v[162:163]
	v_pk_mul_f32 v[154:155], v[154:155], v[166:167] op_sel_hi:[1,0]
	v_rcp_f32_e32 v166, v170
	v_pk_mul_f32 v[160:161], v[130:131], v[160:161]
	v_div_scale_f32 v171, vcc, 1.0, v167, 1.0
	v_pk_mul_f32 v[152:153], v[152:153], v[160:161]
	v_exp_f32_e32 v160, v168
	v_fma_f32 v168, -v170, v166, 1.0
	v_fmac_f32_e32 v166, v168, v166
	v_mul_f32_e32 v168, v171, v166
	v_exp_f32_e32 v161, v169
	v_fma_f32 v169, -v170, v168, v171
	v_exp_f32_e32 v156, v156
	v_exp_f32_e32 v157, v157
	v_fmac_f32_e32 v168, v169, v166
	v_fma_f32 v169, -v170, v168, v171
	v_div_fmas_f32 v166, v169, v166, v168
	v_div_fixup_f32 v166, v166, v167, 1.0
	v_exp_f32_e32 v150, v150
	v_exp_f32_e32 v151, v151
	v_exp_f32_e32 v154, v154
	v_exp_f32_e32 v155, v155
	v_pk_fma_f32 v[160:161], v[166:167], v[160:161], v[166:167] op_sel_hi:[0,1,0]
	v_pk_fma_f32 v[156:157], v[166:167], v[156:157], v[166:167] op_sel_hi:[0,1,0]
	v_rcp_f32_e32 v160, v160
	v_rcp_f32_e32 v161, v161
	v_rcp_f32_e32 v156, v156
	v_rcp_f32_e32 v157, v157
	v_pk_fma_f32 v[150:151], v[166:167], v[150:151], v[166:167] op_sel_hi:[0,1,0]
	v_pk_fma_f32 v[154:155], v[166:167], v[154:155], v[166:167] op_sel_hi:[0,1,0]
	v_rcp_f32_e32 v150, v150
	v_rcp_f32_e32 v151, v151
	v_rcp_f32_e32 v154, v154
	v_rcp_f32_e32 v155, v155
	v_pk_mul_f32 v[148:149], v[148:149], v[160:161]
	v_pk_mul_f32 v[152:153], v[152:153], v[156:157]
	v_med3_f32 v148, v148, s6, v208
	v_med3_f32 v149, v149, s6, v208
	v_med3_f32 v152, v152, s6, v208
	v_med3_f32 v153, v153, s6, v208
	v_cvt_pk_fp8_f32 v164, v148, v149
	v_cvt_pk_fp8_f32 v165, v152, v153
	v_pk_mul_f32 v[150:151], v[158:159], v[150:151]
	v_pk_mul_f32 v[154:155], v[162:163], v[154:155]
	v_med3_f32 v150, v150, s6, v208
	v_med3_f32 v151, v151, s6, v208
	v_med3_f32 v148, v154, s6, v208
	v_med3_f32 v149, v155, s6, v208
	v_cvt_pk_fp8_f32 v164, v150, v151 op_sel:[0,0,1]
	v_cvt_pk_fp8_f32 v165, v148, v149 op_sel:[0,0,1]
	s_lshl_b64 s[30:31], s[2:3], 14
	v_lshl_add_u64 v[148:149], v[196:197], 0, s[30:31]
	v_cvt_f32_i32_e32 v151, v51
	global_store_dwordx2 v[148:149], v[164:165], off
	v_cvt_f32_i32_e32 v150, v50
	v_cvt_f32_i32_e32 v153, v53
	v_cvt_f32_i32_e32 v152, v52
	v_cvt_f32_i32_e32 v155, v63
	v_cvt_f32_i32_e32 v154, v62
	v_cvt_f32_i32_e32 v157, v65
	v_cvt_f32_i32_e32 v156, v64
	v_cvt_f32_i32_e32 v159, v55
	v_cvt_f32_i32_e32 v158, v54
	v_cvt_f32_i32_e32 v161, v57
	v_cvt_f32_i32_e32 v160, v56
	v_cvt_f32_i32_e32 v163, v67
	v_cvt_f32_i32_e32 v162, v66
	v_cvt_f32_i32_e32 v165, v69
	v_cvt_f32_i32_e32 v164, v68
	v_pk_mul_f32 v[152:153], v[144:145], v[152:153]
	v_pk_mul_f32 v[150:151], v[142:143], v[150:151]
	v_pk_mul_f32 v[156:157], v[136:137], v[156:157]
	v_pk_mul_f32 v[154:155], v[134:135], v[154:155]
	v_pk_mul_f32 v[160:161], v[140:141], v[160:161]
	v_pk_mul_f32 v[158:159], v[138:139], v[158:159]
	v_pk_mul_f32 v[164:165], v[132:133], v[164:165]
	v_pk_mul_f32 v[162:163], v[130:131], v[162:163]
	v_pk_mul_f32 v[160:161], v[152:153], v[160:161]
	v_pk_mul_f32 v[158:159], v[150:151], v[158:159]
	v_pk_mul_f32 v[164:165], v[156:157], v[164:165]
	v_pk_mul_f32 v[162:163], v[154:155], v[162:163]
	v_mov_b32_e32 v166, 0
	v_mov_b32_e32 v167, 0
	s_add_i32 s2, s2, 44
	s_ashr_i32 s3, s2, 31
	s_lshl_b64 s[2:3], s[2:3], 14
	v_mov_b32_e32 v169, v233
	v_mul_f32_e32 v168, 0xbfb8aa3b, v169
	v_mul_f32_e32 v169, v169, v169
	v_div_scale_f32 v170, s[30:31], v169, v169, 1.0
	v_pk_mul_f32 v[150:151], v[150:151], v[168:169] op_sel_hi:[1,0]
	v_pk_mul_f32 v[152:153], v[152:153], v[168:169] op_sel_hi:[1,0]
	v_pk_mul_f32 v[154:155], v[154:155], v[168:169] op_sel_hi:[1,0]
	v_pk_mul_f32 v[156:157], v[156:157], v[168:169] op_sel_hi:[1,0]
	v_rcp_f32_e32 v168, v170
	v_div_scale_f32 v171, vcc, 1.0, v169, 1.0
	v_exp_f32_e32 v150, v150
	v_fma_f32 v172, -v170, v168, 1.0
	v_fmac_f32_e32 v168, v172, v168
	v_mul_f32_e32 v172, v171, v168
	v_fma_f32 v173, -v170, v172, v171
	v_exp_f32_e32 v151, v151
	v_exp_f32_e32 v154, v154
	v_exp_f32_e32 v155, v155
	v_fmac_f32_e32 v172, v173, v168
	v_fma_f32 v170, -v170, v172, v171
	v_div_fmas_f32 v168, v170, v168, v172
	v_div_fixup_f32 v168, v168, v169, 1.0
	v_exp_f32_e32 v152, v152
	v_exp_f32_e32 v153, v153
	v_exp_f32_e32 v156, v156
	v_exp_f32_e32 v157, v157
	v_pk_fma_f32 v[150:151], v[168:169], v[150:151], v[168:169] op_sel_hi:[0,1,0]
	v_pk_fma_f32 v[154:155], v[168:169], v[154:155], v[168:169] op_sel_hi:[0,1,0]
	v_rcp_f32_e32 v150, v150
	v_rcp_f32_e32 v151, v151
	v_rcp_f32_e32 v154, v154
	v_rcp_f32_e32 v155, v155
	v_pk_fma_f32 v[152:153], v[168:169], v[152:153], v[168:169] op_sel_hi:[0,1,0]
	v_pk_fma_f32 v[156:157], v[168:169], v[156:157], v[168:169] op_sel_hi:[0,1,0]
	v_rcp_f32_e32 v152, v152
	v_rcp_f32_e32 v153, v153
	v_rcp_f32_e32 v156, v156
	v_rcp_f32_e32 v157, v157
	v_pk_mul_f32 v[150:151], v[158:159], v[150:151]
	v_pk_mul_f32 v[154:155], v[162:163], v[154:155]
	v_med3_f32 v150, v150, s6, v208
	v_med3_f32 v151, v151, s6, v208
	v_med3_f32 v154, v154, s6, v208
	v_med3_f32 v155, v155, s6, v208
	v_cvt_pk_fp8_f32 v166, v150, v151
	v_cvt_pk_fp8_f32 v167, v154, v155
	v_pk_mul_f32 v[152:153], v[160:161], v[152:153]
	v_pk_mul_f32 v[156:157], v[164:165], v[156:157]
	v_med3_f32 v152, v152, s6, v208
	v_med3_f32 v153, v153, s6, v208
	v_med3_f32 v150, v156, s6, v208
	v_med3_f32 v151, v157, s6, v208
	v_cvt_pk_fp8_f32 v166, v152, v153 op_sel:[0,0,1]
	v_cvt_pk_fp8_f32 v167, v150, v151 op_sel:[0,0,1]
	v_cvt_f32_i32_e32 v151, v83
	v_cvt_f32_i32_e32 v150, v82
	v_cvt_f32_i32_e32 v153, v85
	global_store_dwordx2 v[148:149], v[166:167], off offset:2048
	v_cvt_f32_i32_e32 v152, v84
	v_cvt_f32_i32_e32 v155, v95
	v_cvt_f32_i32_e32 v154, v94
	v_cvt_f32_i32_e32 v157, v97
	v_cvt_f32_i32_e32 v156, v96
	v_cvt_f32_i32_e32 v159, v87
	v_cvt_f32_i32_e32 v158, v86
	v_cvt_f32_i32_e32 v161, v89
	v_cvt_f32_i32_e32 v160, v88
	v_cvt_f32_i32_e32 v163, v99
	v_cvt_f32_i32_e32 v162, v98
	v_cvt_f32_i32_e32 v165, v101
	v_cvt_f32_i32_e32 v164, v100
	v_pk_mul_f32 v[152:153], v[144:145], v[152:153]
	v_pk_mul_f32 v[150:151], v[142:143], v[150:151]
	v_pk_mul_f32 v[156:157], v[136:137], v[156:157]
	v_pk_mul_f32 v[154:155], v[134:135], v[154:155]
	v_pk_mul_f32 v[160:161], v[140:141], v[160:161]
	v_pk_mul_f32 v[158:159], v[138:139], v[158:159]
	v_pk_mul_f32 v[164:165], v[132:133], v[164:165]
	v_pk_mul_f32 v[162:163], v[130:131], v[162:163]
	v_pk_mul_f32 v[160:161], v[152:153], v[160:161]
	v_pk_mul_f32 v[158:159], v[150:151], v[158:159]
	v_pk_mul_f32 v[164:165], v[156:157], v[164:165]
	v_pk_mul_f32 v[162:163], v[154:155], v[162:163]
	v_mov_b32_e32 v166, 0
	v_mov_b32_e32 v167, 0
	v_mov_b32_e32 v169, v234
	v_mul_f32_e32 v168, 0xbfb8aa3b, v169
	v_mul_f32_e32 v169, v169, v169
	v_div_scale_f32 v170, s[30:31], v169, v169, 1.0
	v_pk_mul_f32 v[150:151], v[150:151], v[168:169] op_sel_hi:[1,0]
	v_pk_mul_f32 v[152:153], v[152:153], v[168:169] op_sel_hi:[1,0]
	v_pk_mul_f32 v[154:155], v[154:155], v[168:169] op_sel_hi:[1,0]
	v_pk_mul_f32 v[156:157], v[156:157], v[168:169] op_sel_hi:[1,0]
	v_rcp_f32_e32 v168, v170
	v_div_scale_f32 v171, vcc, 1.0, v169, 1.0
	v_exp_f32_e32 v150, v150
	v_fma_f32 v172, -v170, v168, 1.0
	v_fmac_f32_e32 v168, v172, v168
	v_mul_f32_e32 v172, v171, v168
	v_fma_f32 v173, -v170, v172, v171
	v_exp_f32_e32 v151, v151
	v_exp_f32_e32 v154, v154
	v_exp_f32_e32 v155, v155
	v_fmac_f32_e32 v172, v173, v168
	v_fma_f32 v170, -v170, v172, v171
	v_div_fmas_f32 v168, v170, v168, v172
	v_div_fixup_f32 v168, v168, v169, 1.0
	v_exp_f32_e32 v152, v152
	v_exp_f32_e32 v153, v153
	v_exp_f32_e32 v156, v156
	v_exp_f32_e32 v157, v157
	v_pk_fma_f32 v[150:151], v[168:169], v[150:151], v[168:169] op_sel_hi:[0,1,0]
	v_pk_fma_f32 v[154:155], v[168:169], v[154:155], v[168:169] op_sel_hi:[0,1,0]
	v_rcp_f32_e32 v150, v150
	v_rcp_f32_e32 v151, v151
	v_rcp_f32_e32 v154, v154
	v_rcp_f32_e32 v155, v155
	v_pk_fma_f32 v[152:153], v[168:169], v[152:153], v[168:169] op_sel_hi:[0,1,0]
	v_pk_fma_f32 v[156:157], v[168:169], v[156:157], v[168:169] op_sel_hi:[0,1,0]
	v_rcp_f32_e32 v152, v152
	v_rcp_f32_e32 v153, v153
	v_rcp_f32_e32 v156, v156
	v_rcp_f32_e32 v157, v157
	v_pk_mul_f32 v[150:151], v[158:159], v[150:151]
	v_pk_mul_f32 v[154:155], v[162:163], v[154:155]
	v_med3_f32 v150, v150, s6, v208
	v_med3_f32 v151, v151, s6, v208
	v_med3_f32 v154, v154, s6, v208
	v_med3_f32 v155, v155, s6, v208
	v_cvt_pk_fp8_f32 v166, v150, v151
	v_cvt_pk_fp8_f32 v167, v154, v155
	v_pk_mul_f32 v[152:153], v[160:161], v[152:153]
	v_pk_mul_f32 v[156:157], v[164:165], v[156:157]
	v_med3_f32 v152, v152, s6, v208
	v_med3_f32 v153, v153, s6, v208
	v_med3_f32 v150, v156, s6, v208
	v_med3_f32 v151, v157, s6, v208
	v_cvt_pk_fp8_f32 v166, v152, v153 op_sel:[0,0,1]
	v_cvt_pk_fp8_f32 v167, v150, v151 op_sel:[0,0,1]
	v_add_co_u32_e32 v148, vcc, s71, v148
	v_cvt_f32_i32_e32 v151, v115
	s_nop 0
	v_addc_co_u32_e32 v149, vcc, 0, v149, vcc
	global_store_dwordx2 v[148:149], v[166:167], off
	v_cvt_f32_i32_e32 v150, v114
	v_cvt_f32_i32_e32 v153, v117
	v_cvt_f32_i32_e32 v152, v116
	v_cvt_f32_i32_e32 v155, v123
	v_cvt_f32_i32_e32 v154, v122
	v_cvt_f32_i32_e32 v157, v125
	v_cvt_f32_i32_e32 v156, v124
	v_cvt_f32_i32_e32 v159, v119
	v_cvt_f32_i32_e32 v158, v118
	v_cvt_f32_i32_e32 v161, v121
	v_cvt_f32_i32_e32 v160, v120
	v_cvt_f32_i32_e32 v163, v127
	v_cvt_f32_i32_e32 v162, v126
	v_cvt_f32_i32_e32 v165, v129
	v_cvt_f32_i32_e32 v164, v128
	v_pk_mul_f32 v[152:153], v[144:145], v[152:153]
	v_pk_mul_f32 v[150:151], v[142:143], v[150:151]
	v_pk_mul_f32 v[156:157], v[136:137], v[156:157]
	v_pk_mul_f32 v[154:155], v[134:135], v[154:155]
	v_pk_mul_f32 v[160:161], v[140:141], v[160:161]
	v_pk_mul_f32 v[158:159], v[138:139], v[158:159]
	v_pk_mul_f32 v[164:165], v[132:133], v[164:165]
	v_pk_mul_f32 v[162:163], v[130:131], v[162:163]
	v_pk_mul_f32 v[160:161], v[152:153], v[160:161]
	v_pk_mul_f32 v[158:159], v[150:151], v[158:159]
	v_pk_mul_f32 v[164:165], v[156:157], v[164:165]
	v_pk_mul_f32 v[162:163], v[154:155], v[162:163]
	v_mov_b32_e32 v166, 0
	v_mov_b32_e32 v167, 0
	v_mov_b32_e32 v169, v235
	v_mul_f32_e32 v168, 0xbfb8aa3b, v169
	v_mul_f32_e32 v169, v169, v169
	v_div_scale_f32 v170, s[30:31], v169, v169, 1.0
	v_pk_mul_f32 v[150:151], v[150:151], v[168:169] op_sel_hi:[1,0]
	v_pk_mul_f32 v[152:153], v[152:153], v[168:169] op_sel_hi:[1,0]
	v_pk_mul_f32 v[154:155], v[154:155], v[168:169] op_sel_hi:[1,0]
	v_pk_mul_f32 v[156:157], v[156:157], v[168:169] op_sel_hi:[1,0]
	v_rcp_f32_e32 v168, v170
	v_div_scale_f32 v171, vcc, 1.0, v169, 1.0
	v_exp_f32_e32 v150, v150
	v_fma_f32 v172, -v170, v168, 1.0
	v_fmac_f32_e32 v168, v172, v168
	v_mul_f32_e32 v172, v171, v168
	v_fma_f32 v173, -v170, v172, v171
	v_exp_f32_e32 v151, v151
	v_exp_f32_e32 v154, v154
	v_exp_f32_e32 v155, v155
	v_fmac_f32_e32 v172, v173, v168
	v_fma_f32 v170, -v170, v172, v171
	v_div_fmas_f32 v168, v170, v168, v172
	v_div_fixup_f32 v168, v168, v169, 1.0
	v_exp_f32_e32 v152, v152
	v_exp_f32_e32 v153, v153
	v_exp_f32_e32 v156, v156
	v_exp_f32_e32 v157, v157
	v_pk_fma_f32 v[150:151], v[168:169], v[150:151], v[168:169] op_sel_hi:[0,1,0]
	v_pk_fma_f32 v[154:155], v[168:169], v[154:155], v[168:169] op_sel_hi:[0,1,0]
	v_rcp_f32_e32 v150, v150
	v_rcp_f32_e32 v151, v151
	v_rcp_f32_e32 v154, v154
	v_rcp_f32_e32 v155, v155
	v_pk_fma_f32 v[152:153], v[168:169], v[152:153], v[168:169] op_sel_hi:[0,1,0]
	v_pk_fma_f32 v[156:157], v[168:169], v[156:157], v[168:169] op_sel_hi:[0,1,0]
	v_rcp_f32_e32 v152, v152
	v_rcp_f32_e32 v153, v153
	v_rcp_f32_e32 v156, v156
	v_rcp_f32_e32 v157, v157
	v_pk_mul_f32 v[150:151], v[158:159], v[150:151]
	v_pk_mul_f32 v[154:155], v[162:163], v[154:155]
	v_med3_f32 v150, v150, s6, v208
	v_med3_f32 v151, v151, s6, v208
	v_med3_f32 v154, v154, s6, v208
	v_med3_f32 v155, v155, s6, v208
	v_cvt_pk_fp8_f32 v166, v150, v151
	v_cvt_pk_fp8_f32 v167, v154, v155
	v_pk_mul_f32 v[152:153], v[160:161], v[152:153]
	v_pk_mul_f32 v[156:157], v[164:165], v[156:157]
	v_med3_f32 v152, v152, s6, v208
	v_med3_f32 v153, v153, s6, v208
	v_med3_f32 v150, v156, s6, v208
	v_med3_f32 v151, v157, s6, v208
	v_cvt_pk_fp8_f32 v166, v152, v153 op_sel:[0,0,1]
	v_cvt_pk_fp8_f32 v167, v150, v151 op_sel:[0,0,1]
	v_cvt_f32_i32_e32 v151, v5
	v_cvt_f32_i32_e32 v150, v4
	v_cvt_f32_i32_e32 v153, v7
	global_store_dwordx2 v[148:149], v[166:167], off offset:2048
	v_cvt_f32_i32_e32 v149, v3
	v_cvt_f32_i32_e32 v148, v2
	v_cvt_f32_i32_e32 v152, v6
	v_cvt_f32_i32_e32 v155, v9
	v_cvt_f32_i32_e32 v154, v8
	v_cvt_f32_i32_e32 v157, v11
	v_cvt_f32_i32_e32 v156, v10
	v_cvt_f32_i32_e32 v159, v13
	v_cvt_f32_i32_e32 v158, v12
	v_cvt_f32_i32_e32 v161, v15
	v_cvt_f32_i32_e32 v160, v14
	v_cvt_f32_i32_e32 v163, v17
	v_cvt_f32_i32_e32 v162, v16
	v_pk_mul_f32 v[150:151], v[144:145], v[150:151]
	v_pk_mul_f32 v[148:149], v[142:143], v[148:149]
	v_pk_mul_f32 v[154:155], v[136:137], v[154:155]
	v_pk_mul_f32 v[152:153], v[134:135], v[152:153]
	v_pk_mul_f32 v[158:159], v[140:141], v[158:159]
	v_pk_mul_f32 v[156:157], v[138:139], v[156:157]
	v_pk_mul_f32 v[162:163], v[132:133], v[162:163]
	v_pk_mul_f32 v[160:161], v[130:131], v[160:161]
	v_pk_mul_f32 v[158:159], v[150:151], v[158:159]
	v_pk_mul_f32 v[156:157], v[148:149], v[156:157]
	v_pk_mul_f32 v[162:163], v[154:155], v[162:163]
	v_pk_mul_f32 v[160:161], v[152:153], v[160:161]
	v_mov_b32_e32 v164, 0
	v_mov_b32_e32 v165, 0
	v_mov_b32_e32 v167, v236
	v_mul_f32_e32 v166, 0xbfb8aa3b, v167
	v_mul_f32_e32 v167, v167, v167
	v_div_scale_f32 v168, s[30:31], v167, v167, 1.0
	v_pk_mul_f32 v[148:149], v[148:149], v[166:167] op_sel_hi:[1,0]
	v_pk_mul_f32 v[150:151], v[150:151], v[166:167] op_sel_hi:[1,0]
	v_pk_mul_f32 v[152:153], v[152:153], v[166:167] op_sel_hi:[1,0]
	v_pk_mul_f32 v[154:155], v[154:155], v[166:167] op_sel_hi:[1,0]
	v_rcp_f32_e32 v166, v168
	v_div_scale_f32 v169, vcc, 1.0, v167, 1.0
	v_exp_f32_e32 v148, v148
	v_fma_f32 v170, -v168, v166, 1.0
	v_fmac_f32_e32 v166, v170, v166
	v_mul_f32_e32 v170, v169, v166
	v_fma_f32 v171, -v168, v170, v169
	v_exp_f32_e32 v149, v149
	v_exp_f32_e32 v152, v152
	v_exp_f32_e32 v153, v153
	v_fmac_f32_e32 v170, v171, v166
	v_fma_f32 v168, -v168, v170, v169
	v_div_fmas_f32 v166, v168, v166, v170
	v_div_fixup_f32 v166, v166, v167, 1.0
	v_exp_f32_e32 v150, v150
	v_exp_f32_e32 v151, v151
	v_exp_f32_e32 v154, v154
	v_exp_f32_e32 v155, v155
	v_pk_fma_f32 v[148:149], v[166:167], v[148:149], v[166:167] op_sel_hi:[0,1,0]
	v_pk_fma_f32 v[152:153], v[166:167], v[152:153], v[166:167] op_sel_hi:[0,1,0]
	v_rcp_f32_e32 v148, v148
	v_rcp_f32_e32 v149, v149
	v_rcp_f32_e32 v152, v152
	v_rcp_f32_e32 v153, v153
	v_pk_fma_f32 v[150:151], v[166:167], v[150:151], v[166:167] op_sel_hi:[0,1,0]
	v_pk_fma_f32 v[154:155], v[166:167], v[154:155], v[166:167] op_sel_hi:[0,1,0]
	v_rcp_f32_e32 v150, v150
	v_rcp_f32_e32 v151, v151
	v_rcp_f32_e32 v154, v154
	v_rcp_f32_e32 v155, v155
	v_pk_mul_f32 v[148:149], v[156:157], v[148:149]
	v_pk_mul_f32 v[152:153], v[160:161], v[152:153]
	v_med3_f32 v148, v148, s6, v208
	v_med3_f32 v149, v149, s6, v208
	v_med3_f32 v152, v152, s6, v208
	v_med3_f32 v153, v153, s6, v208
	v_cvt_pk_fp8_f32 v164, v148, v149
	v_cvt_pk_fp8_f32 v165, v152, v153
	v_pk_mul_f32 v[150:151], v[158:159], v[150:151]
	v_pk_mul_f32 v[154:155], v[162:163], v[154:155]
	v_med3_f32 v150, v150, s6, v208
	v_med3_f32 v151, v151, s6, v208
	v_med3_f32 v148, v154, s6, v208
	v_med3_f32 v149, v155, s6, v208
	v_cvt_pk_fp8_f32 v164, v150, v151 op_sel:[0,0,1]
	v_cvt_pk_fp8_f32 v165, v148, v149 op_sel:[0,0,1]
	v_lshl_add_u64 v[148:149], v[196:197], 0, s[2:3]
	v_cvt_f32_i32_e32 v151, v31
	v_cvt_f32_i32_e32 v150, v30
	global_store_dwordx2 v[148:149], v[164:165], off
	v_cvt_f32_i32_e32 v153, v33
	v_cvt_f32_i32_e32 v152, v32
	v_cvt_f32_i32_e32 v155, v43
	v_cvt_f32_i32_e32 v154, v42
	v_cvt_f32_i32_e32 v157, v45
	v_cvt_f32_i32_e32 v156, v44
	v_cvt_f32_i32_e32 v159, v39
	v_cvt_f32_i32_e32 v158, v38
	v_cvt_f32_i32_e32 v161, v41
	v_cvt_f32_i32_e32 v160, v40
	v_cvt_f32_i32_e32 v163, v47
	v_cvt_f32_i32_e32 v162, v46
	v_cvt_f32_i32_e32 v165, v49
	v_cvt_f32_i32_e32 v164, v48
	v_pk_mul_f32 v[152:153], v[144:145], v[152:153]
	v_pk_mul_f32 v[150:151], v[142:143], v[150:151]
	v_pk_mul_f32 v[156:157], v[136:137], v[156:157]
	v_pk_mul_f32 v[154:155], v[134:135], v[154:155]
	v_pk_mul_f32 v[160:161], v[140:141], v[160:161]
	v_pk_mul_f32 v[158:159], v[138:139], v[158:159]
	v_pk_mul_f32 v[164:165], v[132:133], v[164:165]
	v_pk_mul_f32 v[162:163], v[130:131], v[162:163]
	v_pk_mul_f32 v[160:161], v[152:153], v[160:161]
	v_pk_mul_f32 v[158:159], v[150:151], v[158:159]
	v_pk_mul_f32 v[164:165], v[156:157], v[164:165]
	v_pk_mul_f32 v[162:163], v[154:155], v[162:163]
	v_mov_b32_e32 v166, 0
	v_mov_b32_e32 v167, 0
	v_mov_b32_e32 v169, v237
	v_mul_f32_e32 v168, 0xbfb8aa3b, v169
	v_mul_f32_e32 v169, v169, v169
	v_div_scale_f32 v170, s[2:3], v169, v169, 1.0
	v_pk_mul_f32 v[150:151], v[150:151], v[168:169] op_sel_hi:[1,0]
	v_pk_mul_f32 v[152:153], v[152:153], v[168:169] op_sel_hi:[1,0]
	v_pk_mul_f32 v[154:155], v[154:155], v[168:169] op_sel_hi:[1,0]
	v_pk_mul_f32 v[156:157], v[156:157], v[168:169] op_sel_hi:[1,0]
	v_rcp_f32_e32 v168, v170
	v_div_scale_f32 v171, vcc, 1.0, v169, 1.0
	v_exp_f32_e32 v150, v150
	v_fma_f32 v172, -v170, v168, 1.0
	v_fmac_f32_e32 v168, v172, v168
	v_mul_f32_e32 v172, v171, v168
	v_fma_f32 v173, -v170, v172, v171
	v_exp_f32_e32 v151, v151
	v_exp_f32_e32 v154, v154
	v_exp_f32_e32 v155, v155
	v_fmac_f32_e32 v172, v173, v168
	v_fma_f32 v170, -v170, v172, v171
	v_div_fmas_f32 v168, v170, v168, v172
	v_div_fixup_f32 v168, v168, v169, 1.0
	v_exp_f32_e32 v152, v152
	v_exp_f32_e32 v153, v153
	v_exp_f32_e32 v156, v156
	v_exp_f32_e32 v157, v157
	v_pk_fma_f32 v[150:151], v[168:169], v[150:151], v[168:169] op_sel_hi:[0,1,0]
	v_pk_fma_f32 v[154:155], v[168:169], v[154:155], v[168:169] op_sel_hi:[0,1,0]
	v_rcp_f32_e32 v150, v150
	v_rcp_f32_e32 v151, v151
	v_rcp_f32_e32 v154, v154
	v_rcp_f32_e32 v155, v155
	v_pk_fma_f32 v[152:153], v[168:169], v[152:153], v[168:169] op_sel_hi:[0,1,0]
	v_pk_fma_f32 v[156:157], v[168:169], v[156:157], v[168:169] op_sel_hi:[0,1,0]
	v_rcp_f32_e32 v152, v152
	v_rcp_f32_e32 v153, v153
	v_rcp_f32_e32 v156, v156
	v_rcp_f32_e32 v157, v157
	v_pk_mul_f32 v[150:151], v[158:159], v[150:151]
	v_pk_mul_f32 v[154:155], v[162:163], v[154:155]
	v_med3_f32 v150, v150, s6, v208
	v_med3_f32 v151, v151, s6, v208
	v_med3_f32 v154, v154, s6, v208
	v_med3_f32 v155, v155, s6, v208
	v_cvt_pk_fp8_f32 v166, v150, v151
	v_cvt_pk_fp8_f32 v167, v154, v155
	v_pk_mul_f32 v[152:153], v[160:161], v[152:153]
	v_pk_mul_f32 v[156:157], v[164:165], v[156:157]
	v_med3_f32 v152, v152, s6, v208
	v_med3_f32 v153, v153, s6, v208
	v_med3_f32 v150, v156, s6, v208
	v_med3_f32 v151, v157, s6, v208
	v_cvt_pk_fp8_f32 v166, v152, v153 op_sel:[0,0,1]
	v_cvt_pk_fp8_f32 v167, v150, v151 op_sel:[0,0,1]
	v_cvt_f32_i32_e32 v151, v59
	v_cvt_f32_i32_e32 v150, v58
	v_cvt_f32_i32_e32 v153, v61
	global_store_dwordx2 v[148:149], v[166:167], off offset:2048
	v_cvt_f32_i32_e32 v152, v60
	v_cvt_f32_i32_e32 v155, v75
	v_cvt_f32_i32_e32 v154, v74
	v_cvt_f32_i32_e32 v157, v77
	v_cvt_f32_i32_e32 v156, v76
	v_cvt_f32_i32_e32 v159, v71
	v_cvt_f32_i32_e32 v158, v70
	v_cvt_f32_i32_e32 v161, v73
	v_cvt_f32_i32_e32 v160, v72
	v_cvt_f32_i32_e32 v163, v79
	v_cvt_f32_i32_e32 v162, v78
	v_cvt_f32_i32_e32 v165, v81
	v_cvt_f32_i32_e32 v164, v80
	v_pk_mul_f32 v[152:153], v[144:145], v[152:153]
	v_pk_mul_f32 v[150:151], v[142:143], v[150:151]
	v_pk_mul_f32 v[156:157], v[136:137], v[156:157]
	v_pk_mul_f32 v[154:155], v[134:135], v[154:155]
	v_pk_mul_f32 v[160:161], v[140:141], v[160:161]
	v_pk_mul_f32 v[158:159], v[138:139], v[158:159]
	v_pk_mul_f32 v[164:165], v[132:133], v[164:165]
	v_pk_mul_f32 v[162:163], v[130:131], v[162:163]
	v_pk_mul_f32 v[160:161], v[152:153], v[160:161]
	v_pk_mul_f32 v[158:159], v[150:151], v[158:159]
	v_pk_mul_f32 v[164:165], v[156:157], v[164:165]
	v_pk_mul_f32 v[162:163], v[154:155], v[162:163]
	v_mov_b32_e32 v166, 0
	v_mov_b32_e32 v167, 0
	v_mov_b32_e32 v169, v238
	v_mul_f32_e32 v168, 0xbfb8aa3b, v169
	v_mul_f32_e32 v169, v169, v169
	v_div_scale_f32 v170, s[2:3], v169, v169, 1.0
	v_pk_mul_f32 v[150:151], v[150:151], v[168:169] op_sel_hi:[1,0]
	v_pk_mul_f32 v[152:153], v[152:153], v[168:169] op_sel_hi:[1,0]
	v_pk_mul_f32 v[154:155], v[154:155], v[168:169] op_sel_hi:[1,0]
	v_pk_mul_f32 v[156:157], v[156:157], v[168:169] op_sel_hi:[1,0]
	v_rcp_f32_e32 v168, v170
	v_div_scale_f32 v171, vcc, 1.0, v169, 1.0
	v_exp_f32_e32 v150, v150
	v_fma_f32 v172, -v170, v168, 1.0
	v_fmac_f32_e32 v168, v172, v168
	v_mul_f32_e32 v172, v171, v168
	v_fma_f32 v173, -v170, v172, v171
	v_exp_f32_e32 v151, v151
	v_exp_f32_e32 v154, v154
	v_exp_f32_e32 v155, v155
	v_fmac_f32_e32 v172, v173, v168
	v_fma_f32 v170, -v170, v172, v171
	v_div_fmas_f32 v168, v170, v168, v172
	v_div_fixup_f32 v168, v168, v169, 1.0
	v_exp_f32_e32 v152, v152
	v_exp_f32_e32 v153, v153
	v_exp_f32_e32 v156, v156
	v_exp_f32_e32 v157, v157
	v_pk_fma_f32 v[150:151], v[168:169], v[150:151], v[168:169] op_sel_hi:[0,1,0]
	v_pk_fma_f32 v[154:155], v[168:169], v[154:155], v[168:169] op_sel_hi:[0,1,0]
	v_rcp_f32_e32 v150, v150
	v_rcp_f32_e32 v151, v151
	v_rcp_f32_e32 v154, v154
	v_rcp_f32_e32 v155, v155
	v_pk_fma_f32 v[152:153], v[168:169], v[152:153], v[168:169] op_sel_hi:[0,1,0]
	v_pk_fma_f32 v[156:157], v[168:169], v[156:157], v[168:169] op_sel_hi:[0,1,0]
	v_rcp_f32_e32 v152, v152
	v_rcp_f32_e32 v153, v153
	v_rcp_f32_e32 v156, v156
	v_rcp_f32_e32 v157, v157
	v_pk_mul_f32 v[150:151], v[158:159], v[150:151]
	v_pk_mul_f32 v[154:155], v[162:163], v[154:155]
	v_med3_f32 v150, v150, s6, v208
	v_med3_f32 v151, v151, s6, v208
	v_med3_f32 v154, v154, s6, v208
	v_med3_f32 v155, v155, s6, v208
	v_cvt_pk_fp8_f32 v166, v150, v151
	v_cvt_pk_fp8_f32 v167, v154, v155
	v_pk_mul_f32 v[152:153], v[160:161], v[152:153]
	v_pk_mul_f32 v[156:157], v[164:165], v[156:157]
	v_med3_f32 v152, v152, s6, v208
	v_med3_f32 v153, v153, s6, v208
	v_med3_f32 v150, v156, s6, v208
	v_med3_f32 v151, v157, s6, v208
	v_cvt_pk_fp8_f32 v166, v152, v153 op_sel:[0,0,1]
	v_cvt_pk_fp8_f32 v167, v150, v151 op_sel:[0,0,1]
	v_add_co_u32_e32 v148, vcc, s71, v148
	v_cvt_f32_i32_e32 v151, v93
	s_nop 0
	v_addc_co_u32_e32 v149, vcc, 0, v149, vcc
	global_store_dwordx2 v[148:149], v[166:167], off
	v_cvt_f32_i32_e32 v147, v91
	v_cvt_f32_i32_e32 v146, v90
	v_cvt_f32_i32_e32 v150, v92
	v_cvt_f32_i32_e32 v153, v107
	v_cvt_f32_i32_e32 v152, v106
	v_cvt_f32_i32_e32 v155, v109
	v_cvt_f32_i32_e32 v154, v108
	v_cvt_f32_i32_e32 v157, v103
	v_cvt_f32_i32_e32 v156, v102
	v_cvt_f32_i32_e32 v159, v105
	v_cvt_f32_i32_e32 v158, v104
	v_cvt_f32_i32_e32 v161, v111
	v_cvt_f32_i32_e32 v160, v110
	v_cvt_f32_i32_e32 v163, v113
	v_cvt_f32_i32_e32 v162, v112
	v_pk_mul_f32 v[142:143], v[142:143], v[146:147]
	v_pk_mul_f32 v[144:145], v[144:145], v[150:151]
	v_pk_mul_f32 v[136:137], v[136:137], v[154:155]
	v_pk_mul_f32 v[134:135], v[134:135], v[152:153]
	v_pk_mul_f32 v[140:141], v[140:141], v[158:159]
	v_pk_mul_f32 v[138:139], v[138:139], v[156:157]
	v_pk_mul_f32 v[132:133], v[132:133], v[162:163]
	v_pk_mul_f32 v[130:131], v[130:131], v[160:161]
	v_pk_mul_f32 v[140:141], v[144:145], v[140:141]
	v_pk_mul_f32 v[138:139], v[142:143], v[138:139]
	v_pk_mul_f32 v[132:133], v[136:137], v[132:133]
	v_pk_mul_f32 v[130:131], v[134:135], v[130:131]
	v_mov_b32_e32 v164, 0
	v_mov_b32_e32 v165, 0
	v_mov_b32_e32 v166, v239
	v_mul_f32_e32 v147, v166, v166
	v_mul_f32_e32 v146, 0xbfb8aa3b, v166
	v_div_scale_f32 v150, s[2:3], v147, v147, 1.0
	v_pk_mul_f32 v[142:143], v[142:143], v[146:147] op_sel_hi:[1,0]
	v_pk_mul_f32 v[144:145], v[144:145], v[146:147] op_sel_hi:[1,0]
	v_pk_mul_f32 v[134:135], v[134:135], v[146:147] op_sel_hi:[1,0]
	v_pk_mul_f32 v[136:137], v[136:137], v[146:147] op_sel_hi:[1,0]
	v_rcp_f32_e32 v146, v150
	v_div_scale_f32 v151, vcc, 1.0, v147, 1.0
	v_exp_f32_e32 v142, v142
	v_fma_f32 v152, -v150, v146, 1.0
	v_fmac_f32_e32 v146, v152, v146
	v_mul_f32_e32 v152, v151, v146
	v_fma_f32 v153, -v150, v152, v151
	v_exp_f32_e32 v143, v143
	v_exp_f32_e32 v134, v134
	v_exp_f32_e32 v135, v135
	v_fmac_f32_e32 v152, v153, v146
	v_fma_f32 v150, -v150, v152, v151
	v_div_fmas_f32 v146, v150, v146, v152
	v_div_fixup_f32 v146, v146, v147, 1.0
	v_exp_f32_e32 v144, v144
	v_exp_f32_e32 v145, v145
	v_exp_f32_e32 v136, v136
	v_exp_f32_e32 v137, v137
	v_pk_fma_f32 v[142:143], v[146:147], v[142:143], v[146:147] op_sel_hi:[0,1,0]
	v_pk_fma_f32 v[134:135], v[146:147], v[134:135], v[146:147] op_sel_hi:[0,1,0]
	v_rcp_f32_e32 v142, v142
	v_rcp_f32_e32 v143, v143
	v_rcp_f32_e32 v134, v134
	v_rcp_f32_e32 v135, v135
	v_pk_fma_f32 v[144:145], v[146:147], v[144:145], v[146:147] op_sel_hi:[0,1,0]
	v_pk_fma_f32 v[136:137], v[146:147], v[136:137], v[146:147] op_sel_hi:[0,1,0]
	v_rcp_f32_e32 v144, v144
	v_rcp_f32_e32 v145, v145
	v_rcp_f32_e32 v136, v136
	v_rcp_f32_e32 v137, v137
	v_pk_mul_f32 v[138:139], v[138:139], v[142:143]
	v_pk_mul_f32 v[130:131], v[130:131], v[134:135]
	v_med3_f32 v134, v138, s6, v208
	v_med3_f32 v135, v139, s6, v208
	v_med3_f32 v130, v130, s6, v208
	v_med3_f32 v131, v131, s6, v208
	v_cvt_pk_fp8_f32 v164, v134, v135
	v_cvt_pk_fp8_f32 v165, v130, v131
	v_pk_mul_f32 v[140:141], v[140:141], v[144:145]
	v_pk_mul_f32 v[132:133], v[132:133], v[136:137]
	v_med3_f32 v136, v140, s6, v208
	v_med3_f32 v137, v141, s6, v208
	v_med3_f32 v130, v132, s6, v208
	v_med3_f32 v131, v133, s6, v208
	v_cvt_pk_fp8_f32 v164, v136, v137 op_sel:[0,0,1]
	v_cvt_pk_fp8_f32 v165, v130, v131 op_sel:[0,0,1]
	s_andn2_b64 vcc, exec, s[28:29]
	s_mov_b64 s[2:3], -1
	global_store_dwordx2 v[148:149], v[164:165], off offset:2048
	s_cbranch_vccnz .LBB0_845
	s_andn2_b64 vcc, exec, s[4:5]
	s_cbranch_vccnz .LBB0_844
	s_barrier
	s_branch .LBB0_844

.LBB0_1100:
	v_lshl_or_b32 v148, s79, 8, v203
	v_lshl_add_u32 v150, s76, 8, v201
	v_ashrrev_i32_e32 v149, 31, v148
	v_ashrrev_i32_e32 v151, 31, v150
	s_nop 15
	s_nop 7
	v_lshl_add_u64 v[130:131], v[148:149], 2, s[8:9]
	v_lshl_add_u64 v[146:147], v[150:151], 2, s[38:39]
	global_load_dword v154, v[146:147], off
	global_load_dword v233, v[146:147], off offset:64
	global_load_dword v234, v[146:147], off offset:128
	global_load_dword v235, v[146:147], off offset:192
	global_load_dword v236, v[146:147], off offset:512
	global_load_dword v237, v[146:147], off offset:576
	global_load_dword v238, v[146:147], off offset:640
	global_load_dword v239, v[146:147], off offset:704
	global_load_dwordx4 v[142:145], v[130:131], off
	global_load_dwordx4 v[138:141], v[130:131], off offset:16
	global_load_dwordx4 v[134:137], v[130:131], off offset:512
	s_nop 0
	global_load_dwordx4 v[130:133], v[130:131], off offset:528
	v_cvt_f32_i32_e32 v157, v19
	v_cvt_f32_i32_e32 v156, v18
	v_cvt_f32_i32_e32 v159, v21
	v_cvt_f32_i32_e32 v158, v20
	v_cvt_f32_i32_e32 v161, v23
	v_cvt_f32_i32_e32 v160, v22
	v_cvt_f32_i32_e32 v163, v25
	v_cvt_f32_i32_e32 v162, v24
	v_cvt_f32_i32_e32 v165, v27
	v_cvt_f32_i32_e32 v164, v26
	v_cvt_f32_i32_e32 v167, v29
	v_cvt_f32_i32_e32 v166, v28
	v_cvt_f32_i32_e32 v169, v35
	v_cvt_f32_i32_e32 v168, v34
	v_cvt_f32_i32_e32 v171, v37
	v_cvt_f32_i32_e32 v170, v36
	v_lshlrev_b64 v[174:175], 12, v[150:151]
	v_or_b32_e32 v172, 16, v150
	v_lshlrev_b64 v[152:153], 1, v[148:149]
	v_lshl_add_u64 v[148:149], s[36:37], 0, v[174:175]
	v_ashrrev_i32_e32 v173, 31, v172
	v_lshl_add_u64 v[148:149], v[148:149], 0, v[152:153]
	v_lshl_add_u64 v[174:175], v[172:173], 2, s[38:39]
	v_lshlrev_b64 v[172:173], 12, v[172:173]
	v_lshl_add_u64 v[172:173], s[36:37], 0, v[172:173]
	v_lshl_add_u64 v[172:173], v[172:173], 0, v[152:153]
	s_mov_b32 s28, 0x80000
	s_mov_b64 s[2:3], 0x80000
	s_waitcnt vmcnt(0)
	v_pk_mul_f32 v[176:177], v[142:143], v[154:155] op_sel_hi:[1,0]
	v_pk_mul_f32 v[178:179], v[144:145], v[154:155] op_sel_hi:[1,0]
	v_pk_mul_f32 v[180:181], v[138:139], v[154:155] op_sel_hi:[1,0]
	v_pk_mul_f32 v[182:183], v[140:141], v[154:155] op_sel_hi:[1,0]
	v_pk_mul_f32 v[184:185], v[134:135], v[154:155] op_sel_hi:[1,0]
	v_pk_mul_f32 v[186:187], v[136:137], v[154:155] op_sel_hi:[1,0]
	v_pk_mul_f32 v[188:189], v[130:131], v[154:155] op_sel_hi:[1,0]
	v_pk_mul_f32 v[154:155], v[132:133], v[154:155] op_sel_hi:[1,0]
	v_pk_mul_f32 v[158:159], v[178:179], v[158:159]
	v_pk_mul_f32 v[156:157], v[176:177], v[156:157]
	v_pk_mul_f32 v[162:163], v[182:183], v[162:163]
	v_pk_mul_f32 v[160:161], v[180:181], v[160:161]
	v_pk_mul_f32 v[166:167], v[186:187], v[166:167]
	v_pk_mul_f32 v[164:165], v[184:185], v[164:165]
	v_pk_mul_f32 v[170:171], v[154:155], v[170:171]
	v_pk_mul_f32 v[168:169], v[188:189], v[168:169]
	v_cvt_pk_bf16_f32 v154, v156, v157
	v_cvt_pk_bf16_f32 v155, v158, v159
	v_cvt_pk_bf16_f32 v156, v160, v161
	v_cvt_pk_bf16_f32 v157, v162, v163
	v_cvt_pk_bf16_f32 v158, v164, v165
	v_cvt_pk_bf16_f32 v159, v166, v167
	v_cvt_pk_bf16_f32 v160, v168, v169
	v_cvt_pk_bf16_f32 v161, v170, v171
	global_store_dwordx4 v[148:149], v[154:157], off
	global_store_dwordx4 v[148:149], v[158:161], off offset:256
	v_cvt_f32_i32_e32 v157, v51
	v_cvt_f32_i32_e32 v156, v50
	v_cvt_f32_i32_e32 v159, v53
	v_cvt_f32_i32_e32 v158, v52
	v_cvt_f32_i32_e32 v161, v63
	v_cvt_f32_i32_e32 v160, v62
	v_cvt_f32_i32_e32 v163, v65
	v_cvt_f32_i32_e32 v162, v64
	v_cvt_f32_i32_e32 v165, v55
	v_cvt_f32_i32_e32 v164, v54
	v_cvt_f32_i32_e32 v167, v57
	v_cvt_f32_i32_e32 v166, v56
	v_cvt_f32_i32_e32 v169, v67
	v_cvt_f32_i32_e32 v168, v66
	v_cvt_f32_i32_e32 v171, v69
	v_cvt_f32_i32_e32 v170, v68
	v_or_b32_e32 v174, 32, v150
	v_ashrrev_i32_e32 v175, 31, v174
	v_lshl_add_u64 v[176:177], v[174:175], 2, s[38:39]
	v_or_b32_e32 v150, 48, v150
	v_ashrrev_i32_e32 v151, 31, v150
	v_mov_b32_e32 v154, v233
	v_pk_mul_f32 v[178:179], v[142:143], v[154:155] op_sel_hi:[1,0]
	v_pk_mul_f32 v[180:181], v[144:145], v[154:155] op_sel_hi:[1,0]
	v_pk_mul_f32 v[182:183], v[138:139], v[154:155] op_sel_hi:[1,0]
	v_pk_mul_f32 v[184:185], v[140:141], v[154:155] op_sel_hi:[1,0]
	v_pk_mul_f32 v[186:187], v[134:135], v[154:155] op_sel_hi:[1,0]
	v_pk_mul_f32 v[188:189], v[136:137], v[154:155] op_sel_hi:[1,0]
	v_pk_mul_f32 v[190:191], v[130:131], v[154:155] op_sel_hi:[1,0]
	v_pk_mul_f32 v[154:155], v[132:133], v[154:155] op_sel_hi:[1,0]
	v_pk_mul_f32 v[158:159], v[180:181], v[158:159]
	v_pk_mul_f32 v[156:157], v[178:179], v[156:157]
	v_pk_mul_f32 v[162:163], v[184:185], v[162:163]
	v_pk_mul_f32 v[160:161], v[182:183], v[160:161]
	v_pk_mul_f32 v[166:167], v[188:189], v[166:167]
	v_pk_mul_f32 v[164:165], v[186:187], v[164:165]
	v_pk_mul_f32 v[170:171], v[154:155], v[170:171]
	v_pk_mul_f32 v[168:169], v[190:191], v[168:169]
	v_cvt_pk_bf16_f32 v154, v156, v157
	v_cvt_pk_bf16_f32 v155, v158, v159
	v_cvt_pk_bf16_f32 v156, v160, v161
	v_cvt_pk_bf16_f32 v157, v162, v163
	v_cvt_pk_bf16_f32 v158, v164, v165
	v_cvt_pk_bf16_f32 v159, v166, v167
	v_cvt_pk_bf16_f32 v160, v168, v169
	v_cvt_pk_bf16_f32 v161, v170, v171
	global_store_dwordx4 v[172:173], v[154:157], off
	global_store_dwordx4 v[172:173], v[158:161], off offset:256
	v_cvt_f32_i32_e32 v157, v83
	v_cvt_f32_i32_e32 v156, v82
	v_cvt_f32_i32_e32 v159, v85
	v_cvt_f32_i32_e32 v158, v84
	v_cvt_f32_i32_e32 v161, v95
	v_cvt_f32_i32_e32 v160, v94
	v_cvt_f32_i32_e32 v163, v97
	v_cvt_f32_i32_e32 v162, v96
	v_cvt_f32_i32_e32 v165, v87
	v_cvt_f32_i32_e32 v164, v86
	v_cvt_f32_i32_e32 v167, v89
	v_cvt_f32_i32_e32 v166, v88
	v_cvt_f32_i32_e32 v169, v99
	v_cvt_f32_i32_e32 v168, v98
	v_cvt_f32_i32_e32 v171, v101
	v_cvt_f32_i32_e32 v170, v100
	v_lshlrev_b64 v[172:173], 12, v[174:175]
	v_lshl_add_u64 v[172:173], s[36:37], 0, v[172:173]
	v_lshl_add_u64 v[172:173], v[172:173], 0, v[152:153]
	v_lshl_add_u64 v[174:175], v[150:151], 2, s[38:39]
	v_lshlrev_b64 v[150:151], 12, v[150:151]
	v_lshl_add_u64 v[150:151], s[36:37], 0, v[150:151]
	v_mov_b32_e32 v154, v234
	v_pk_mul_f32 v[176:177], v[142:143], v[154:155] op_sel_hi:[1,0]
	v_pk_mul_f32 v[178:179], v[144:145], v[154:155] op_sel_hi:[1,0]
	v_pk_mul_f32 v[180:181], v[138:139], v[154:155] op_sel_hi:[1,0]
	v_pk_mul_f32 v[182:183], v[140:141], v[154:155] op_sel_hi:[1,0]
	v_pk_mul_f32 v[184:185], v[134:135], v[154:155] op_sel_hi:[1,0]
	v_pk_mul_f32 v[186:187], v[136:137], v[154:155] op_sel_hi:[1,0]
	v_pk_mul_f32 v[188:189], v[130:131], v[154:155] op_sel_hi:[1,0]
	v_pk_mul_f32 v[154:155], v[132:133], v[154:155] op_sel_hi:[1,0]
	v_pk_mul_f32 v[158:159], v[178:179], v[158:159]
	v_pk_mul_f32 v[156:157], v[176:177], v[156:157]
	v_pk_mul_f32 v[162:163], v[182:183], v[162:163]
	v_pk_mul_f32 v[160:161], v[180:181], v[160:161]
	v_pk_mul_f32 v[166:167], v[186:187], v[166:167]
	v_pk_mul_f32 v[164:165], v[184:185], v[164:165]
	v_pk_mul_f32 v[170:171], v[154:155], v[170:171]
	v_pk_mul_f32 v[168:169], v[188:189], v[168:169]
	v_cvt_pk_bf16_f32 v154, v156, v157
	v_cvt_pk_bf16_f32 v155, v158, v159
	v_cvt_pk_bf16_f32 v156, v160, v161
	v_cvt_pk_bf16_f32 v157, v162, v163
	v_cvt_pk_bf16_f32 v158, v164, v165
	v_cvt_pk_bf16_f32 v159, v166, v167
	v_cvt_pk_bf16_f32 v160, v168, v169
	v_cvt_pk_bf16_f32 v161, v170, v171
	global_store_dwordx4 v[172:173], v[154:157], off
	global_store_dwordx4 v[172:173], v[158:161], off offset:256
	v_cvt_f32_i32_e32 v157, v115
	v_cvt_f32_i32_e32 v156, v114
	v_cvt_f32_i32_e32 v159, v117
	v_cvt_f32_i32_e32 v158, v116
	v_cvt_f32_i32_e32 v161, v123
	v_cvt_f32_i32_e32 v160, v122
	v_cvt_f32_i32_e32 v163, v125
	v_cvt_f32_i32_e32 v162, v124
	v_cvt_f32_i32_e32 v165, v119
	v_cvt_f32_i32_e32 v164, v118
	v_cvt_f32_i32_e32 v167, v121
	v_cvt_f32_i32_e32 v166, v120
	v_cvt_f32_i32_e32 v169, v127
	v_cvt_f32_i32_e32 v168, v126
	v_cvt_f32_i32_e32 v171, v129
	v_cvt_f32_i32_e32 v170, v128
	v_lshl_add_u64 v[172:173], v[150:151], 0, v[152:153]
	v_mov_b32_e32 v154, v235
	v_pk_mul_f32 v[150:151], v[142:143], v[154:155] op_sel_hi:[1,0]
	v_pk_mul_f32 v[152:153], v[144:145], v[154:155] op_sel_hi:[1,0]
	v_pk_mul_f32 v[174:175], v[138:139], v[154:155] op_sel_hi:[1,0]
	v_pk_mul_f32 v[176:177], v[140:141], v[154:155] op_sel_hi:[1,0]
	v_pk_mul_f32 v[178:179], v[134:135], v[154:155] op_sel_hi:[1,0]
	v_pk_mul_f32 v[180:181], v[136:137], v[154:155] op_sel_hi:[1,0]
	v_pk_mul_f32 v[182:183], v[130:131], v[154:155] op_sel_hi:[1,0]
	v_pk_mul_f32 v[154:155], v[132:133], v[154:155] op_sel_hi:[1,0]
	v_pk_mul_f32 v[152:153], v[152:153], v[158:159]
	v_pk_mul_f32 v[150:151], v[150:151], v[156:157]
	v_pk_mul_f32 v[156:157], v[176:177], v[162:163]
	v_pk_mul_f32 v[158:159], v[174:175], v[160:161]
	v_pk_mul_f32 v[160:161], v[180:181], v[166:167]
	v_pk_mul_f32 v[162:163], v[178:179], v[164:165]
	v_pk_mul_f32 v[164:165], v[154:155], v[170:171]
	v_pk_mul_f32 v[166:167], v[182:183], v[168:169]
	v_cvt_pk_bf16_f32 v150, v150, v151
	v_cvt_pk_bf16_f32 v151, v152, v153
	v_cvt_pk_bf16_f32 v152, v158, v159
	v_cvt_pk_bf16_f32 v153, v156, v157
	v_cvt_pk_bf16_f32 v154, v162, v163
	v_cvt_pk_bf16_f32 v155, v160, v161
	v_cvt_pk_bf16_f32 v156, v166, v167
	v_cvt_pk_bf16_f32 v157, v164, v165
	global_store_dwordx4 v[172:173], v[150:153], off
	global_store_dwordx4 v[172:173], v[154:157], off offset:256
	v_cvt_f32_i32_e32 v153, v3
	v_cvt_f32_i32_e32 v152, v2
	v_cvt_f32_i32_e32 v155, v5
	v_cvt_f32_i32_e32 v154, v4
	v_cvt_f32_i32_e32 v157, v7
	v_cvt_f32_i32_e32 v156, v6
	v_cvt_f32_i32_e32 v159, v9
	v_cvt_f32_i32_e32 v158, v8
	v_cvt_f32_i32_e32 v161, v11
	v_cvt_f32_i32_e32 v160, v10
	v_cvt_f32_i32_e32 v163, v13
	v_cvt_f32_i32_e32 v162, v12
	v_cvt_f32_i32_e32 v165, v15
	v_cvt_f32_i32_e32 v164, v14
	v_cvt_f32_i32_e32 v167, v17
	v_cvt_f32_i32_e32 v166, v16
	v_add_co_u32_e32 v170, vcc, s28, v148
	v_lshl_add_u64 v[168:169], v[148:149], 0, s[2:3]
	s_nop 0
	v_addc_co_u32_e32 v171, vcc, 0, v149, vcc
	s_mov_b32 s28, 0x90000
	s_mov_b64 s[2:3], 0x90000
	v_mov_b32_e32 v150, v236
	v_pk_mul_f32 v[172:173], v[142:143], v[150:151] op_sel_hi:[1,0]
	v_pk_mul_f32 v[174:175], v[144:145], v[150:151] op_sel_hi:[1,0]
	v_pk_mul_f32 v[176:177], v[138:139], v[150:151] op_sel_hi:[1,0]
	v_pk_mul_f32 v[178:179], v[140:141], v[150:151] op_sel_hi:[1,0]
	v_pk_mul_f32 v[180:181], v[134:135], v[150:151] op_sel_hi:[1,0]
	v_pk_mul_f32 v[182:183], v[136:137], v[150:151] op_sel_hi:[1,0]
	v_pk_mul_f32 v[184:185], v[130:131], v[150:151] op_sel_hi:[1,0]
	v_pk_mul_f32 v[150:151], v[132:133], v[150:151] op_sel_hi:[1,0]
	v_pk_mul_f32 v[154:155], v[174:175], v[154:155]
	v_pk_mul_f32 v[152:153], v[172:173], v[152:153]
	v_pk_mul_f32 v[158:159], v[178:179], v[158:159]
	v_pk_mul_f32 v[156:157], v[176:177], v[156:157]
	v_pk_mul_f32 v[162:163], v[182:183], v[162:163]
	v_pk_mul_f32 v[160:161], v[180:181], v[160:161]
	v_pk_mul_f32 v[166:167], v[150:151], v[166:167]
	v_pk_mul_f32 v[164:165], v[184:185], v[164:165]
	v_cvt_pk_bf16_f32 v150, v152, v153
	v_cvt_pk_bf16_f32 v151, v154, v155
	v_cvt_pk_bf16_f32 v152, v156, v157
	v_cvt_pk_bf16_f32 v153, v158, v159
	v_cvt_pk_bf16_f32 v154, v160, v161
	v_cvt_pk_bf16_f32 v155, v162, v163
	v_cvt_pk_bf16_f32 v156, v164, v165
	v_cvt_pk_bf16_f32 v157, v166, v167
	global_store_dwordx4 v[170:171], v[150:153], off
	global_store_dwordx4 v[168:169], v[154:157], off offset:256
	v_cvt_f32_i32_e32 v153, v31
	v_cvt_f32_i32_e32 v152, v30
	v_cvt_f32_i32_e32 v155, v33
	v_cvt_f32_i32_e32 v154, v32
	v_cvt_f32_i32_e32 v157, v43
	v_cvt_f32_i32_e32 v156, v42
	v_cvt_f32_i32_e32 v159, v45
	v_cvt_f32_i32_e32 v158, v44
	v_cvt_f32_i32_e32 v161, v39
	v_cvt_f32_i32_e32 v160, v38
	v_cvt_f32_i32_e32 v163, v41
	v_cvt_f32_i32_e32 v162, v40
	v_cvt_f32_i32_e32 v165, v47
	v_cvt_f32_i32_e32 v164, v46
	v_cvt_f32_i32_e32 v167, v49
	v_cvt_f32_i32_e32 v166, v48
	v_add_co_u32_e32 v170, vcc, s28, v148
	v_lshl_add_u64 v[168:169], v[148:149], 0, s[2:3]
	s_nop 0
	v_addc_co_u32_e32 v171, vcc, 0, v149, vcc
	s_mov_b32 s28, 0xa0000
	s_mov_b64 s[2:3], 0xa0000
	v_mov_b32_e32 v150, v237
	v_pk_mul_f32 v[172:173], v[142:143], v[150:151] op_sel_hi:[1,0]
	v_pk_mul_f32 v[174:175], v[144:145], v[150:151] op_sel_hi:[1,0]
	v_pk_mul_f32 v[176:177], v[138:139], v[150:151] op_sel_hi:[1,0]
	v_pk_mul_f32 v[178:179], v[140:141], v[150:151] op_sel_hi:[1,0]
	v_pk_mul_f32 v[180:181], v[134:135], v[150:151] op_sel_hi:[1,0]
	v_pk_mul_f32 v[182:183], v[136:137], v[150:151] op_sel_hi:[1,0]
	v_pk_mul_f32 v[184:185], v[130:131], v[150:151] op_sel_hi:[1,0]
	v_pk_mul_f32 v[150:151], v[132:133], v[150:151] op_sel_hi:[1,0]
	v_pk_mul_f32 v[154:155], v[174:175], v[154:155]
	v_pk_mul_f32 v[152:153], v[172:173], v[152:153]
	v_pk_mul_f32 v[158:159], v[178:179], v[158:159]
	v_pk_mul_f32 v[156:157], v[176:177], v[156:157]
	v_pk_mul_f32 v[162:163], v[182:183], v[162:163]
	v_pk_mul_f32 v[160:161], v[180:181], v[160:161]
	v_pk_mul_f32 v[166:167], v[150:151], v[166:167]
	v_pk_mul_f32 v[164:165], v[184:185], v[164:165]
	v_cvt_pk_bf16_f32 v150, v152, v153
	v_cvt_pk_bf16_f32 v151, v154, v155
	v_cvt_pk_bf16_f32 v152, v156, v157
	v_cvt_pk_bf16_f32 v153, v158, v159
	v_cvt_pk_bf16_f32 v154, v160, v161
	v_cvt_pk_bf16_f32 v155, v162, v163
	v_cvt_pk_bf16_f32 v156, v164, v165
	v_cvt_pk_bf16_f32 v157, v166, v167
	global_store_dwordx4 v[170:171], v[150:153], off
	global_store_dwordx4 v[168:169], v[154:157], off offset:256
	v_cvt_f32_i32_e32 v153, v59
	v_cvt_f32_i32_e32 v152, v58
	v_cvt_f32_i32_e32 v155, v61
	v_cvt_f32_i32_e32 v154, v60
	v_cvt_f32_i32_e32 v157, v75
	v_cvt_f32_i32_e32 v156, v74
	v_cvt_f32_i32_e32 v159, v77
	v_cvt_f32_i32_e32 v158, v76
	v_cvt_f32_i32_e32 v161, v71
	v_cvt_f32_i32_e32 v160, v70
	v_cvt_f32_i32_e32 v163, v73
	v_cvt_f32_i32_e32 v162, v72
	v_cvt_f32_i32_e32 v165, v79
	v_cvt_f32_i32_e32 v164, v78
	v_cvt_f32_i32_e32 v167, v81
	v_cvt_f32_i32_e32 v166, v80
	v_add_co_u32_e32 v170, vcc, s28, v148
	v_lshl_add_u64 v[168:169], v[148:149], 0, s[2:3]
	s_nop 0
	v_addc_co_u32_e32 v171, vcc, 0, v149, vcc
	s_andn2_b64 vcc, exec, s[0:1]
	v_mov_b32_e32 v150, v238
	v_pk_mul_f32 v[172:173], v[142:143], v[150:151] op_sel_hi:[1,0]
	v_pk_mul_f32 v[174:175], v[144:145], v[150:151] op_sel_hi:[1,0]
	v_pk_mul_f32 v[176:177], v[138:139], v[150:151] op_sel_hi:[1,0]
	v_pk_mul_f32 v[178:179], v[140:141], v[150:151] op_sel_hi:[1,0]
	v_pk_mul_f32 v[180:181], v[134:135], v[150:151] op_sel_hi:[1,0]
	v_pk_mul_f32 v[182:183], v[136:137], v[150:151] op_sel_hi:[1,0]
	v_pk_mul_f32 v[184:185], v[130:131], v[150:151] op_sel_hi:[1,0]
	v_pk_mul_f32 v[150:151], v[132:133], v[150:151] op_sel_hi:[1,0]
	v_pk_mul_f32 v[154:155], v[174:175], v[154:155]
	v_pk_mul_f32 v[152:153], v[172:173], v[152:153]
	v_pk_mul_f32 v[158:159], v[178:179], v[158:159]
	v_pk_mul_f32 v[156:157], v[176:177], v[156:157]
	v_pk_mul_f32 v[162:163], v[182:183], v[162:163]
	v_pk_mul_f32 v[160:161], v[180:181], v[160:161]
	v_pk_mul_f32 v[166:167], v[150:151], v[166:167]
	v_pk_mul_f32 v[164:165], v[184:185], v[164:165]
	v_cvt_pk_bf16_f32 v150, v152, v153
	v_cvt_pk_bf16_f32 v151, v154, v155
	v_cvt_pk_bf16_f32 v152, v156, v157
	v_cvt_pk_bf16_f32 v153, v158, v159
	v_cvt_pk_bf16_f32 v154, v160, v161
	v_cvt_pk_bf16_f32 v155, v162, v163
	v_cvt_pk_bf16_f32 v156, v164, v165
	v_cvt_pk_bf16_f32 v157, v166, v167
	global_store_dwordx4 v[170:171], v[150:153], off
	global_store_dwordx4 v[168:169], v[154:157], off offset:256
	v_cvt_f32_i32_e32 v151, v91
	v_cvt_f32_i32_e32 v150, v90
	v_cvt_f32_i32_e32 v153, v93
	v_cvt_f32_i32_e32 v152, v92
	v_cvt_f32_i32_e32 v155, v107
	v_cvt_f32_i32_e32 v154, v106
	v_cvt_f32_i32_e32 v157, v109
	v_cvt_f32_i32_e32 v156, v108
	v_cvt_f32_i32_e32 v159, v103
	v_cvt_f32_i32_e32 v158, v102
	v_cvt_f32_i32_e32 v161, v105
	v_cvt_f32_i32_e32 v160, v104
	v_cvt_f32_i32_e32 v163, v111
	v_cvt_f32_i32_e32 v162, v110
	v_cvt_f32_i32_e32 v165, v113
	v_cvt_f32_i32_e32 v164, v112
	v_lshl_add_u64 v[166:167], v[148:149], 0, s[18:19]
	v_add_co_u32_e64 v148, s[0:1], s73, v148
	v_mov_b32_e32 v146, v239
	v_pk_mul_f32 v[142:143], v[142:143], v[146:147] op_sel_hi:[1,0]
	v_pk_mul_f32 v[144:145], v[144:145], v[146:147] op_sel_hi:[1,0]
	v_pk_mul_f32 v[138:139], v[138:139], v[146:147] op_sel_hi:[1,0]
	v_pk_mul_f32 v[140:141], v[140:141], v[146:147] op_sel_hi:[1,0]
	v_addc_co_u32_e64 v149, s[0:1], 0, v149, s[0:1]
	v_pk_mul_f32 v[134:135], v[134:135], v[146:147] op_sel_hi:[1,0]
	v_pk_mul_f32 v[136:137], v[136:137], v[146:147] op_sel_hi:[1,0]
	v_pk_mul_f32 v[130:131], v[130:131], v[146:147] op_sel_hi:[1,0]
	v_pk_mul_f32 v[132:133], v[132:133], v[146:147] op_sel_hi:[1,0]
	v_pk_mul_f32 v[144:145], v[144:145], v[152:153]
	v_pk_mul_f32 v[142:143], v[142:143], v[150:151]
	v_pk_mul_f32 v[140:141], v[140:141], v[156:157]
	v_pk_mul_f32 v[138:139], v[138:139], v[154:155]
	v_pk_mul_f32 v[136:137], v[136:137], v[160:161]
	v_pk_mul_f32 v[134:135], v[134:135], v[158:159]
	v_pk_mul_f32 v[146:147], v[132:133], v[164:165]
	v_pk_mul_f32 v[150:151], v[130:131], v[162:163]
	v_cvt_pk_bf16_f32 v130, v142, v143
	v_cvt_pk_bf16_f32 v131, v144, v145
	v_cvt_pk_bf16_f32 v132, v138, v139
	v_cvt_pk_bf16_f32 v133, v140, v141
	s_mov_b64 s[0:1], -1
	v_cvt_pk_bf16_f32 v134, v134, v135
	v_cvt_pk_bf16_f32 v135, v136, v137
	v_cvt_pk_bf16_f32 v136, v150, v151
	v_cvt_pk_bf16_f32 v137, v146, v147
	global_store_dwordx4 v[148:149], v[130:133], off
	global_store_dwordx4 v[166:167], v[134:137], off offset:256
	s_cbranch_vccnz .LBB0_1082
	s_andn2_b64 vcc, exec, s[6:7]
	s_cbranch_vccnz .LBB0_1081
	s_barrier
	s_branch .LBB0_1081
